# vJ
# speedup vs baseline: 1.0496x; 1.0040x over previous
.LBB1_4:
	s_or_b64 exec, exec, s[2:3]
	s_load_dwordx2 s[12:13], s[0:1], 0x0
	s_mov_b64 s[0:1], src_shared_base
	s_cmp_lg_u32 0, -1
	s_cselect_b32 s0, s1, 0
	s_cselect_b32 s1, 0, 0
	v_mov_b32_e32 v2, s1
	v_mov_b32_e32 v3, s0
	s_waitcnt lgkmcnt(0)
	s_barrier
	flat_load_dword v2, v[2:3] sc0 sc1
	s_waitcnt vmcnt(0)
	s_movk_i32 s2, 0xff
	v_cmp_lt_u32_e32 vcc, s2, v0
	v_lshlrev_b32_e32 v130, 4, v0
	v_lshrrev_b32_e32 v3, 1, v0
	v_bfe_u32 v202, v0, 5, 1
	v_and_b32_e32 v1, 3, v0
	v_and_b32_e32 v4, 64, v130
	v_and_b32_e32 v3, 12, v3
	v_and_b32_e32 v5, 0x1df0, v130
	v_mul_u32_u24_e32 v6, 0x820, v202
	v_or3_b32 v1, v1, v4, v3
	v_lshl_or_b32 v3, v202, 13, v5
	v_lshl_add_u32 v195, v1, 4, v6
	s_mov_b32 s1, 0
	s_movk_i32 s0, 0x820
	v_add_u32_e32 v1, 0, v195
	v_add_u32_e32 v194, 0, v3
	s_waitcnt lgkmcnt(0)
	s_barrier
	v_readfirstlane_b32 s14, v2
	s_ashr_i32 s2, s14, 1
	s_and_b32 s3, s14, 4
	s_and_b32 s2, s2, -8
	s_lshl_b32 s6, s14, 5
	s_or_b32 s2, s2, s3
	s_and_b32 s28, s6, 0x60
	s_ashr_i32 s33, s2, 2
	s_add_i32 s2, s33, s28
	s_ashr_i32 s3, s2, 31
	s_lshl_b64 s[20:21], s[2:3], 7
	s_bfe_u32 s29, s14, 0x10003
	v_lshrrev_b32_e32 v1, 6, v0
	v_and_b32_e32 v240, 31, v0
	v_bfe_u32 v241, v0, 5, 1
	v_readfirstlane_b32 s34, v1
	s_lshl_b32 s35, s20, 12
	s_add_u32 s40, s12, s35
	s_addc_u32 s41, s13, 0
	s_add_u32 s42, s40, 0x10000
	s_addc_u32 s43, s41, 0
	s_add_u32 s44, s42, 0x10000
	s_addc_u32 s45, s43, 0
	s_add_u32 s46, s44, 0x10000
	s_addc_u32 s47, s45, 0
	s_add_u32 s48, s46, 0x10000
	s_addc_u32 s49, s47, 0
	s_add_u32 s50, s48, 0x10000
	s_addc_u32 s51, s49, 0
	s_add_u32 s52, s50, 0x10000
	s_addc_u32 s53, s51, 0
	s_add_u32 s54, s52, 0x10000
	s_addc_u32 s55, s53, 0
	s_lshl_b32 s35, s29, 20
	s_add_u32 s56, s10, s35
	s_addc_u32 s57, s11, 0
	s_lshl_b32 s35, s34, 10
	v_lshlrev_b32_e32 v1, 4, v240
	v_lshl_add_u32 v1, v241, 13, v1
	v_add_u32_e32 v239, s35, v1
	v_bfe_u32 v1, v240, 2, 1
	v_and_b32_e32 v242, 3, v240
	v_lshrrev_b32_e32 v243, 3, v240
	v_lshl_add_u32 v242, v243, 2, v242
	v_lshl_add_u32 v1, v1, 6, v242
	v_mul_u32_u24_e32 v1, 0x110, v1
	v_lshl_add_u32 v236, v241, 4, v1
	v_lshrrev_b32_e32 v1, 5, v0
	v_lshlrev_b32_e32 v242, 12, v1
	v_lshl_add_u32 v238, v240, 4, v242
	v_mul_u32_u24_e32 v242, 0x110, v1
	v_lshl_add_u32 v237, v240, 3, v242
	s_lshl_b32 s35, s29, 9
	v_and_b32_e32 v1, 0x1c0, v0
	v_or3_b32 v1, s35, v1, v240
	v_lshlrev_b32_e32 v1, 2, v1
	global_load_dword v244, v1, s[8:9]
	global_load_dword v245, v1, s[8:9] offset:128
	global_load_dwordx4 v[204:207], v238, s[40:41] nt
	global_load_dwordx4 v[208:211], v238, s[42:43] nt
	global_load_dwordx4 v[212:215], v238, s[44:45] nt
	global_load_dwordx4 v[216:219], v238, s[46:47] nt
	global_load_dwordx4 v[220:223], v238, s[48:49] nt
	global_load_dwordx4 v[224:227], v238, s[50:51] nt
	global_load_dwordx4 v[228:231], v238, s[52:53] nt
	global_load_dwordx4 v[232:235], v238, s[54:55] nt
	global_load_dwordx4 v[146:149], v239, s[56:57]
	global_load_dwordx4 v[150:153], v239, s[56:57] offset:512
	s_add_u32 s56, s56, 0x4000
	s_addc_u32 s57, s57, 0
	global_load_dwordx4 v[154:157], v239, s[56:57]
	global_load_dwordx4 v[158:161], v239, s[56:57] offset:512
	s_add_u32 s56, s56, 0x4000
	s_addc_u32 s57, s57, 0
	global_load_dwordx4 v[162:165], v239, s[56:57]
	global_load_dwordx4 v[166:169], v239, s[56:57] offset:512
	s_add_u32 s56, s56, 0x4000
	s_addc_u32 s57, s57, 0
	global_load_dwordx4 v[170:173], v239, s[56:57]
	global_load_dwordx4 v[174:177], v239, s[56:57] offset:512
	s_add_u32 s56, s56, 0x4000
	s_addc_u32 s57, s57, 0
	global_load_dwordx4 v[178:181], v239, s[56:57]
	global_load_dwordx4 v[182:185], v239, s[56:57] offset:512
	s_add_u32 s56, s56, 0x4000
	s_addc_u32 s57, s57, 0
	global_load_dwordx4 v[186:189], v239, s[56:57]
	global_load_dwordx4 v[190:193], v239, s[56:57] offset:512
	s_add_u32 s56, s56, 0x4000
	s_addc_u32 s57, s57, 0
	global_load_dwordx4 v[194:197], v239, s[56:57]
	global_load_dwordx4 v[198:201], v239, s[56:57] offset:512
	s_add_u32 s56, s56, 0x4000
	s_addc_u32 s57, s57, 0
	s_waitcnt vmcnt(22)
	s_mov_b32 s38, 0x41a00000
	s_mov_b32 s58, 0
.Lsp_loop:
	v_mov_b32_e32 v3, v244
	v_cmp_nlt_f32_e32 vcc, s38, v3
	s_and_saveexec_b64 s[36:37], vcc
	s_cbranch_execz .Lsp_skip
	v_mul_f32_e32 v2, 0x3fb8aa3b, v3
	s_mov_b32 s39, 0x3fb8aa3b
	v_rndne_f32_e32 v4, v2
	v_sub_f32_e32 v5, v2, v4
	v_fma_f32 v2, v3, s39, -v2
	v_fmamk_f32 v2, v3, 0x32a5705f, v2
	v_add_f32_e32 v2, v5, v2
	v_exp_f32_e32 v2, v2
	v_cvt_i32_f32_e32 v4, v4
	s_mov_b32 s39, 0xc2ce8ed0
	v_cmp_ngt_f32_e32 vcc, s39, v3
	s_mov_b32 s39, 0x42b17218
	v_ldexp_f32 v2, v2, v4
	v_cndmask_b32_e32 v2, 0, v2, vcc
	v_mov_b32_e32 v16, 0x7f800000
	v_cmp_nlt_f32_e32 vcc, s39, v3
	s_mov_b32 s39, 0x3f2aaaab
	s_mov_b32 s35, 0x7f800000
	v_cndmask_b32_e32 v17, v16, v2, vcc
	v_add_f32_e32 v4, 1.0, v17
	v_add_f32_e32 v2, -1.0, v4
	v_sub_f32_e32 v3, v2, v4
	v_add_f32_e32 v3, 1.0, v3
	v_sub_f32_e32 v2, v17, v2
	v_add_f32_e32 v5, v2, v3
	v_frexp_mant_f32_e32 v6, v4
	v_cvt_f64_f32_e32 v[2:3], v4
	v_frexp_exp_i32_f64_e32 v2, v[2:3]
	v_cmp_gt_f32_e32 vcc, s39, v6
	s_mov_b32 s39, 0x3f317218
	s_nop 0
	v_subbrev_co_u32_e32 v10, vcc, 0, v2, vcc
	v_sub_u32_e32 v2, 0, v10
	v_ldexp_f32 v3, v4, v2
	v_add_f32_e32 v4, -1.0, v3
	v_add_f32_e32 v6, 1.0, v3
	v_ldexp_f32 v2, v5, v2
	v_add_f32_e32 v5, 1.0, v4
	v_add_f32_e32 v7, -1.0, v6
	v_sub_f32_e32 v5, v3, v5
	v_sub_f32_e32 v3, v3, v7
	v_add_f32_e32 v5, v2, v5
	v_add_f32_e32 v2, v2, v3
	v_add_f32_e32 v11, v6, v2
	v_rcp_f32_e32 v13, v11
	v_sub_f32_e32 v3, v6, v11
	v_add_f32_e32 v12, v2, v3
	v_add_f32_e32 v3, v4, v5
	v_mul_f32_e32 v15, v3, v13
	v_sub_f32_e32 v2, v4, v3
	v_mul_f32_e32 v4, v11, v15
	v_fma_f32 v6, v15, v11, -v4
	v_fmac_f32_e32 v6, v15, v12
	v_add_f32_e32 v14, v5, v2
	v_add_f32_e32 v2, v4, v6
	v_sub_f32_e32 v5, v3, v2
	v_pk_add_f32 v[8:9], v[2:3], v[4:5] neg_lo:[0,1] neg_hi:[0,1]
	v_mov_b32_e32 v7, v2
	v_pk_add_f32 v[2:3], v[8:9], v[6:7] neg_lo:[0,1] neg_hi:[0,1]
	v_cmp_neq_f32_e32 vcc, s35, v17
	v_add_f32_e32 v3, v14, v3
	v_add_f32_e32 v2, v2, v3
	v_add_f32_e32 v3, v5, v2
	v_mul_f32_e32 v14, v13, v3
	v_mul_f32_e32 v4, v11, v14
	v_fma_f32 v6, v14, v11, -v4
	v_fmac_f32_e32 v6, v14, v12
	v_sub_f32_e32 v5, v5, v3
	v_add_f32_e32 v11, v2, v5
	v_add_f32_e32 v2, v4, v6
	v_sub_f32_e32 v5, v3, v2
	v_pk_add_f32 v[8:9], v[2:3], v[4:5] neg_lo:[0,1] neg_hi:[0,1]
	v_mov_b32_e32 v7, v2
	v_pk_add_f32 v[2:3], v[8:9], v[6:7] neg_lo:[0,1] neg_hi:[0,1]
	v_cvt_f32_i32_e32 v4, v10
	v_add_f32_e32 v3, v11, v3
	v_add_f32_e32 v2, v2, v3
	v_add_f32_e32 v2, v5, v2
	v_add_f32_e32 v5, v15, v14
	v_sub_f32_e32 v3, v5, v15
	v_mul_f32_e32 v2, v13, v2
	v_sub_f32_e32 v3, v14, v3
	v_add_f32_e32 v2, v3, v2
	v_add_f32_e32 v6, v5, v2
	v_mul_f32_e32 v8, v6, v6
	v_mov_b32_e32 v3, 0x3ecc95a3
	v_sub_f32_e32 v5, v6, v5
	v_fmac_f32_e32 v3, 0x3e9b6dac, v8
	v_sub_f32_e32 v2, v2, v5
	v_fmaak_f32 v3, v8, v3, 0x3f2aaada
	v_ldexp_f32 v9, v2, 1
	v_mul_f32_e32 v5, v6, v8
	v_mov_b32_e32 v2, 0x3f317218
	v_pk_mul_f32 v[2:3], v[4:5], v[2:3]
	v_ldexp_f32 v7, v6, 1
	v_fma_f32 v5, v4, s39, -v2
	v_fmamk_f32 v6, v4, 0xb102e308, v5
	v_pk_add_f32 v[4:5], v[2:3], v[6:7]
	v_mov_b32_e32 v8, v2
	v_sub_f32_e32 v7, v5, v7
	v_sub_f32_e32 v7, v3, v7
	v_add_f32_e32 v9, v9, v7
	v_pk_add_f32 v[2:3], v[4:5], v[2:3] neg_lo:[0,1] neg_hi:[0,1]
	v_pk_add_f32 v[10:11], v[4:5], v[8:9]
	v_mov_b32_e32 v7, v4
	v_mov_b32_e32 v3, v11
	v_pk_add_f32 v[12:13], v[6:7], v[2:3] neg_lo:[0,1] neg_hi:[0,1]
	v_pk_add_f32 v[2:3], v[6:7], v[2:3]
	v_mov_b32_e32 v8, v9
	v_pk_add_f32 v[6:7], v[2:3], v[4:5] op_sel:[1,0] op_sel_hi:[0,1] neg_lo:[0,1] neg_hi:[0,1]
	v_pk_add_f32 v[14:15], v[10:11], v[6:7] op_sel_hi:[1,0] neg_lo:[0,1] neg_hi:[0,1]
	v_mov_b32_e32 v10, v11
	v_mov_b32_e32 v11, v3
	v_pk_mov_b32 v[6:7], v[4:5], v[6:7] op_sel:[1,0]
	v_mov_b32_e32 v9, v4
	v_pk_add_f32 v[6:7], v[10:11], v[6:7] neg_lo:[0,1] neg_hi:[0,1]
	v_mov_b32_e32 v14, v12
	v_pk_add_f32 v[4:5], v[8:9], v[6:7] neg_lo:[0,1] neg_hi:[0,1]
	v_mov_b32_e32 v13, v3
	v_pk_add_f32 v[6:7], v[14:15], v[4:5]
	s_mov_b32 s39, 0x33800000
	v_pk_add_f32 v[8:9], v[6:7], v[6:7] op_sel:[0,1] op_sel_hi:[1,0]
	s_nop 0
	v_pk_add_f32 v[2:3], v[2:3], v[8:9] op_sel:[1,0] op_sel_hi:[0,1]
	v_mov_b32_e32 v7, v2
	v_pk_add_f32 v[10:11], v[6:7], v[12:13] neg_lo:[0,1] neg_hi:[0,1]
	v_mov_b32_e32 v5, v8
	v_sub_f32_e32 v3, v6, v10
	v_pk_add_f32 v[4:5], v[4:5], v[10:11] neg_lo:[0,1] neg_hi:[0,1]
	v_sub_f32_e32 v3, v12, v3
	v_add_f32_e32 v3, v4, v3
	v_add_f32_e32 v3, v3, v5
	v_add_f32_e32 v2, v2, v3
	v_cndmask_b32_e32 v2, v16, v2, vcc
	v_cmp_lt_f32_e64 vcc, |v17|, s39
	s_nop 1
	v_cndmask_b32_e32 v3, v2, v17, vcc
.Lsp_skip:
	s_or_b64 exec, exec, s[36:37]
	v_mov_b32_e32 v244, v245
	v_mov_b32_e32 v245, v3
	s_add_u32 s58, s58, 1
	s_cmp_lt_u32 s58, 2
	s_cbranch_scc1 .Lsp_loop
	s_waitcnt vmcnt(21)
	v_cvt_pk_f16_f32 v204, v204, v205
	v_cvt_pk_f16_f32 v205, v206, v207
	ds_write_b64 v237, v[204:205]
	s_waitcnt vmcnt(20)
	v_cvt_pk_f16_f32 v208, v208, v209
	v_cvt_pk_f16_f32 v209, v210, v211
	ds_write_b64 v237, v[208:209] offset:4352
	s_waitcnt vmcnt(19)
	v_cvt_pk_f16_f32 v212, v212, v213
	v_cvt_pk_f16_f32 v213, v214, v215
	ds_write_b64 v237, v[212:213] offset:8704
	s_waitcnt vmcnt(18)
	v_cvt_pk_f16_f32 v216, v216, v217
	v_cvt_pk_f16_f32 v217, v218, v219
	ds_write_b64 v237, v[216:217] offset:13056
	s_waitcnt vmcnt(17)
	v_cvt_pk_f16_f32 v220, v220, v221
	v_cvt_pk_f16_f32 v221, v222, v223
	ds_write_b64 v237, v[220:221] offset:17408
	s_waitcnt vmcnt(16)
	v_cvt_pk_f16_f32 v224, v224, v225
	v_cvt_pk_f16_f32 v225, v226, v227
	ds_write_b64 v237, v[224:225] offset:21760
	s_waitcnt vmcnt(15)
	v_cvt_pk_f16_f32 v228, v228, v229
	v_cvt_pk_f16_f32 v229, v230, v231
	ds_write_b64 v237, v[228:229] offset:26112
	s_waitcnt vmcnt(14)
	v_cvt_pk_f16_f32 v232, v232, v233
	v_cvt_pk_f16_f32 v233, v234, v235
	ds_write_b64 v237, v[232:233] offset:30464
	global_load_dwordx4 v[204:207], v238, s[40:41] offset:512 nt
	global_load_dwordx4 v[208:211], v238, s[42:43] offset:512 nt
	global_load_dwordx4 v[212:215], v238, s[44:45] offset:512 nt
	global_load_dwordx4 v[216:219], v238, s[46:47] offset:512 nt
	global_load_dwordx4 v[220:223], v238, s[48:49] offset:512 nt
	global_load_dwordx4 v[224:227], v238, s[50:51] offset:512 nt
	global_load_dwordx4 v[228:231], v238, s[52:53] offset:512 nt
	global_load_dwordx4 v[232:235], v238, s[54:55] offset:512 nt
	s_waitcnt lgkmcnt(0)
	s_barrier
	ds_read_b128 v[130:133], v236
	ds_read_b128 v[134:137], v236 offset:4352
	ds_read_b128 v[138:141], v236 offset:8704
	ds_read_b128 v[142:145], v236 offset:13056
	s_waitcnt vmcnt(20)
	s_waitcnt lgkmcnt(3)
	v_mfma_f32_32x32x16_f16 v[82:97], v[130:133], v[146:149], 0
	v_mfma_f32_32x32x16_f16 v[50:65], v[130:133], v[150:153], 0
	ds_read_b128 v[130:133], v236 offset:32
	s_waitcnt lgkmcnt(3)
	v_mfma_f32_32x32x16_f16 v[114:129], v[134:137], v[146:149], 0
	v_mfma_f32_32x32x16_f16 v[34:49], v[134:137], v[150:153], 0
	ds_read_b128 v[134:137], v236 offset:4384
	s_waitcnt lgkmcnt(3)
	v_mfma_f32_32x32x16_f16 v[98:113], v[138:141], v[146:149], 0
	v_mfma_f32_32x32x16_f16 v[18:33], v[138:141], v[150:153], 0
	ds_read_b128 v[138:141], v236 offset:8736
	s_waitcnt lgkmcnt(3)
	v_mfma_f32_32x32x16_f16 v[66:81], v[142:145], v[146:149], 0
	v_mfma_f32_32x32x16_f16 v[2:17], v[142:145], v[150:153], 0
	ds_read_b128 v[142:145], v236 offset:13088
	global_load_dwordx4 v[146:149], v239, s[56:57]
	global_load_dwordx4 v[150:153], v239, s[56:57] offset:512
	s_add_u32 s56, s56, 0x4000
	s_addc_u32 s57, s57, 0
	s_waitcnt vmcnt(20)
	s_waitcnt lgkmcnt(3)
	v_mfma_f32_32x32x16_f16 v[82:97], v[130:133], v[154:157], v[82:97]
	v_mfma_f32_32x32x16_f16 v[50:65], v[130:133], v[158:161], v[50:65]
	ds_read_b128 v[130:133], v236 offset:64
	s_waitcnt lgkmcnt(3)
	v_mfma_f32_32x32x16_f16 v[114:129], v[134:137], v[154:157], v[114:129]
	v_mfma_f32_32x32x16_f16 v[34:49], v[134:137], v[158:161], v[34:49]
	ds_read_b128 v[134:137], v236 offset:4416
	s_waitcnt lgkmcnt(3)
	v_mfma_f32_32x32x16_f16 v[98:113], v[138:141], v[154:157], v[98:113]
	v_mfma_f32_32x32x16_f16 v[18:33], v[138:141], v[158:161], v[18:33]
	ds_read_b128 v[138:141], v236 offset:8768
	s_waitcnt lgkmcnt(3)
	v_mfma_f32_32x32x16_f16 v[66:81], v[142:145], v[154:157], v[66:81]
	v_mfma_f32_32x32x16_f16 v[2:17], v[142:145], v[158:161], v[2:17]
	ds_read_b128 v[142:145], v236 offset:13120
	global_load_dwordx4 v[154:157], v239, s[56:57]
	global_load_dwordx4 v[158:161], v239, s[56:57] offset:512
	s_add_u32 s56, s56, 0x4000
	s_addc_u32 s57, s57, 0
	s_waitcnt vmcnt(20)
	s_waitcnt lgkmcnt(3)
	v_mfma_f32_32x32x16_f16 v[82:97], v[130:133], v[162:165], v[82:97]
	v_mfma_f32_32x32x16_f16 v[50:65], v[130:133], v[166:169], v[50:65]
	ds_read_b128 v[130:133], v236 offset:96
	s_waitcnt lgkmcnt(3)
	v_mfma_f32_32x32x16_f16 v[114:129], v[134:137], v[162:165], v[114:129]
	v_mfma_f32_32x32x16_f16 v[34:49], v[134:137], v[166:169], v[34:49]
	ds_read_b128 v[134:137], v236 offset:4448
	s_waitcnt lgkmcnt(3)
	v_mfma_f32_32x32x16_f16 v[98:113], v[138:141], v[162:165], v[98:113]
	v_mfma_f32_32x32x16_f16 v[18:33], v[138:141], v[166:169], v[18:33]
	ds_read_b128 v[138:141], v236 offset:8800
	s_waitcnt lgkmcnt(3)
	v_mfma_f32_32x32x16_f16 v[66:81], v[142:145], v[162:165], v[66:81]
	v_mfma_f32_32x32x16_f16 v[2:17], v[142:145], v[166:169], v[2:17]
	ds_read_b128 v[142:145], v236 offset:13152
	global_load_dwordx4 v[162:165], v239, s[56:57]
	global_load_dwordx4 v[166:169], v239, s[56:57] offset:512
	s_add_u32 s56, s56, 0x4000
	s_addc_u32 s57, s57, 0
	s_waitcnt vmcnt(20)
	s_waitcnt lgkmcnt(3)
	v_mfma_f32_32x32x16_f16 v[82:97], v[130:133], v[170:173], v[82:97]
	v_mfma_f32_32x32x16_f16 v[50:65], v[130:133], v[174:177], v[50:65]
	ds_read_b128 v[130:133], v236 offset:128
	s_waitcnt lgkmcnt(3)
	v_mfma_f32_32x32x16_f16 v[114:129], v[134:137], v[170:173], v[114:129]
	v_mfma_f32_32x32x16_f16 v[34:49], v[134:137], v[174:177], v[34:49]
	ds_read_b128 v[134:137], v236 offset:4480
	s_waitcnt lgkmcnt(3)
	v_mfma_f32_32x32x16_f16 v[98:113], v[138:141], v[170:173], v[98:113]
	v_mfma_f32_32x32x16_f16 v[18:33], v[138:141], v[174:177], v[18:33]
	ds_read_b128 v[138:141], v236 offset:8832
	s_waitcnt lgkmcnt(3)
	v_mfma_f32_32x32x16_f16 v[66:81], v[142:145], v[170:173], v[66:81]
	v_mfma_f32_32x32x16_f16 v[2:17], v[142:145], v[174:177], v[2:17]
	ds_read_b128 v[142:145], v236 offset:13184
	global_load_dwordx4 v[170:173], v239, s[56:57]
	global_load_dwordx4 v[174:177], v239, s[56:57] offset:512
	s_add_u32 s56, s56, 0x4000
	s_addc_u32 s57, s57, 0
	s_waitcnt vmcnt(20)
	s_waitcnt lgkmcnt(3)
	v_mfma_f32_32x32x16_f16 v[82:97], v[130:133], v[178:181], v[82:97]
	v_mfma_f32_32x32x16_f16 v[50:65], v[130:133], v[182:185], v[50:65]
	ds_read_b128 v[130:133], v236 offset:160
	s_waitcnt lgkmcnt(3)
	v_mfma_f32_32x32x16_f16 v[114:129], v[134:137], v[178:181], v[114:129]
	v_mfma_f32_32x32x16_f16 v[34:49], v[134:137], v[182:185], v[34:49]
	ds_read_b128 v[134:137], v236 offset:4512
	s_waitcnt lgkmcnt(3)
	v_mfma_f32_32x32x16_f16 v[98:113], v[138:141], v[178:181], v[98:113]
	v_mfma_f32_32x32x16_f16 v[18:33], v[138:141], v[182:185], v[18:33]
	ds_read_b128 v[138:141], v236 offset:8864
	s_waitcnt lgkmcnt(3)
	v_mfma_f32_32x32x16_f16 v[66:81], v[142:145], v[178:181], v[66:81]
	v_mfma_f32_32x32x16_f16 v[2:17], v[142:145], v[182:185], v[2:17]
	ds_read_b128 v[142:145], v236 offset:13216
	global_load_dwordx4 v[178:181], v239, s[56:57]
	global_load_dwordx4 v[182:185], v239, s[56:57] offset:512
	s_add_u32 s56, s56, 0x4000
	s_addc_u32 s57, s57, 0
	s_waitcnt vmcnt(20)
	s_waitcnt lgkmcnt(3)
	v_mfma_f32_32x32x16_f16 v[82:97], v[130:133], v[186:189], v[82:97]
	v_mfma_f32_32x32x16_f16 v[50:65], v[130:133], v[190:193], v[50:65]
	ds_read_b128 v[130:133], v236 offset:192
	s_waitcnt lgkmcnt(3)
	v_mfma_f32_32x32x16_f16 v[114:129], v[134:137], v[186:189], v[114:129]
	v_mfma_f32_32x32x16_f16 v[34:49], v[134:137], v[190:193], v[34:49]
	ds_read_b128 v[134:137], v236 offset:4544
	s_waitcnt lgkmcnt(3)
	v_mfma_f32_32x32x16_f16 v[98:113], v[138:141], v[186:189], v[98:113]
	v_mfma_f32_32x32x16_f16 v[18:33], v[138:141], v[190:193], v[18:33]
	ds_read_b128 v[138:141], v236 offset:8896
	s_waitcnt lgkmcnt(3)
	v_mfma_f32_32x32x16_f16 v[66:81], v[142:145], v[186:189], v[66:81]
	v_mfma_f32_32x32x16_f16 v[2:17], v[142:145], v[190:193], v[2:17]
	ds_read_b128 v[142:145], v236 offset:13248
	global_load_dwordx4 v[186:189], v239, s[56:57]
	global_load_dwordx4 v[190:193], v239, s[56:57] offset:512
	s_add_u32 s56, s56, 0x4000
	s_addc_u32 s57, s57, 0
	s_waitcnt vmcnt(19)
	v_cvt_pk_f16_f32 v204, v204, v205
	v_cvt_pk_f16_f32 v205, v206, v207
	ds_write_b64 v237, v[204:205] offset:34816
	s_waitcnt vmcnt(18)
	v_cvt_pk_f16_f32 v208, v208, v209
	v_cvt_pk_f16_f32 v209, v210, v211
	ds_write_b64 v237, v[208:209] offset:39168
	s_waitcnt vmcnt(17)
	v_cvt_pk_f16_f32 v212, v212, v213
	v_cvt_pk_f16_f32 v213, v214, v215
	ds_write_b64 v237, v[212:213] offset:43520
	s_waitcnt vmcnt(16)
	v_cvt_pk_f16_f32 v216, v216, v217
	v_cvt_pk_f16_f32 v217, v218, v219
	ds_write_b64 v237, v[216:217] offset:47872
	s_waitcnt vmcnt(15)
	v_cvt_pk_f16_f32 v220, v220, v221
	v_cvt_pk_f16_f32 v221, v222, v223
	ds_write_b64 v237, v[220:221] offset:52224
	s_waitcnt vmcnt(14)
	v_cvt_pk_f16_f32 v224, v224, v225
	v_cvt_pk_f16_f32 v225, v226, v227
	ds_write_b64 v237, v[224:225] offset:56576
	s_waitcnt vmcnt(13)
	v_cvt_pk_f16_f32 v228, v228, v229
	v_cvt_pk_f16_f32 v229, v230, v231
	ds_write_b64 v237, v[228:229] offset:60928
	s_waitcnt vmcnt(12)
	v_cvt_pk_f16_f32 v232, v232, v233
	v_cvt_pk_f16_f32 v233, v234, v235
	ds_write_b64 v237, v[232:233] offset:65280
	global_load_dwordx4 v[204:207], v238, s[40:41] offset:1024 nt
	global_load_dwordx4 v[208:211], v238, s[42:43] offset:1024 nt
	global_load_dwordx4 v[212:215], v238, s[44:45] offset:1024 nt
	global_load_dwordx4 v[216:219], v238, s[46:47] offset:1024 nt
	global_load_dwordx4 v[220:223], v238, s[48:49] offset:1024 nt
	global_load_dwordx4 v[224:227], v238, s[50:51] offset:1024 nt
	global_load_dwordx4 v[228:231], v238, s[52:53] offset:1024 nt
	global_load_dwordx4 v[232:235], v238, s[54:55] offset:1024 nt
	s_waitcnt vmcnt(28)
	s_waitcnt lgkmcnt(11)
	v_mfma_f32_32x32x16_f16 v[82:97], v[130:133], v[194:197], v[82:97]
	v_mfma_f32_32x32x16_f16 v[50:65], v[130:133], v[198:201], v[50:65]
	ds_read_b128 v[130:133], v236 offset:224
	s_waitcnt lgkmcnt(11)
	v_mfma_f32_32x32x16_f16 v[114:129], v[134:137], v[194:197], v[114:129]
	v_mfma_f32_32x32x16_f16 v[34:49], v[134:137], v[198:201], v[34:49]
	ds_read_b128 v[134:137], v236 offset:4576
	s_waitcnt lgkmcnt(11)
	v_mfma_f32_32x32x16_f16 v[98:113], v[138:141], v[194:197], v[98:113]
	v_mfma_f32_32x32x16_f16 v[18:33], v[138:141], v[198:201], v[18:33]
	ds_read_b128 v[138:141], v236 offset:8928
	s_waitcnt lgkmcnt(11)
	v_mfma_f32_32x32x16_f16 v[66:81], v[142:145], v[194:197], v[66:81]
	v_mfma_f32_32x32x16_f16 v[2:17], v[142:145], v[198:201], v[2:17]
	ds_read_b128 v[142:145], v236 offset:13280
	global_load_dwordx4 v[194:197], v239, s[56:57]
	global_load_dwordx4 v[198:201], v239, s[56:57] offset:512
	s_add_u32 s56, s56, 0x4000
	s_addc_u32 s57, s57, 0
	s_waitcnt vmcnt(20)
	s_waitcnt lgkmcnt(3)
	v_mfma_f32_32x32x16_f16 v[82:97], v[130:133], v[146:149], v[82:97]
	v_mfma_f32_32x32x16_f16 v[50:65], v[130:133], v[150:153], v[50:65]
	s_waitcnt lgkmcnt(2)
	v_mfma_f32_32x32x16_f16 v[114:129], v[134:137], v[146:149], v[114:129]
	v_mfma_f32_32x32x16_f16 v[34:49], v[134:137], v[150:153], v[34:49]
	s_waitcnt lgkmcnt(1)
	v_mfma_f32_32x32x16_f16 v[98:113], v[138:141], v[146:149], v[98:113]
	v_mfma_f32_32x32x16_f16 v[18:33], v[138:141], v[150:153], v[18:33]
	s_waitcnt lgkmcnt(0)
	v_mfma_f32_32x32x16_f16 v[66:81], v[142:145], v[146:149], v[66:81]
	v_mfma_f32_32x32x16_f16 v[2:17], v[142:145], v[150:153], v[2:17]
	global_load_dwordx4 v[146:149], v239, s[56:57]
	global_load_dwordx4 v[150:153], v239, s[56:57] offset:512
	s_add_u32 s56, s56, 0x4000
	s_addc_u32 s57, s57, 0
	s_waitcnt lgkmcnt(0)
	s_barrier
	ds_read_b128 v[130:133], v236 offset:34816
	ds_read_b128 v[134:137], v236 offset:39168
	ds_read_b128 v[138:141], v236 offset:43520
	ds_read_b128 v[142:145], v236 offset:47872
	s_waitcnt vmcnt(20)
	s_waitcnt lgkmcnt(3)
	v_mfma_f32_32x32x16_f16 v[82:97], v[130:133], v[154:157], v[82:97]
	v_mfma_f32_32x32x16_f16 v[50:65], v[130:133], v[158:161], v[50:65]
	ds_read_b128 v[130:133], v236 offset:34848
	s_waitcnt lgkmcnt(3)
	v_mfma_f32_32x32x16_f16 v[114:129], v[134:137], v[154:157], v[114:129]
	v_mfma_f32_32x32x16_f16 v[34:49], v[134:137], v[158:161], v[34:49]
	ds_read_b128 v[134:137], v236 offset:39200
	s_waitcnt lgkmcnt(3)
	v_mfma_f32_32x32x16_f16 v[98:113], v[138:141], v[154:157], v[98:113]
	v_mfma_f32_32x32x16_f16 v[18:33], v[138:141], v[158:161], v[18:33]
	ds_read_b128 v[138:141], v236 offset:43552
	s_waitcnt lgkmcnt(3)
	v_mfma_f32_32x32x16_f16 v[66:81], v[142:145], v[154:157], v[66:81]
	v_mfma_f32_32x32x16_f16 v[2:17], v[142:145], v[158:161], v[2:17]
	ds_read_b128 v[142:145], v236 offset:47904
	global_load_dwordx4 v[154:157], v239, s[56:57]
	global_load_dwordx4 v[158:161], v239, s[56:57] offset:512
	s_add_u32 s56, s56, 0x4000
	s_addc_u32 s57, s57, 0
	s_waitcnt vmcnt(20)
	s_waitcnt lgkmcnt(3)
	v_mfma_f32_32x32x16_f16 v[82:97], v[130:133], v[162:165], v[82:97]
	v_mfma_f32_32x32x16_f16 v[50:65], v[130:133], v[166:169], v[50:65]
	ds_read_b128 v[130:133], v236 offset:34880
	s_waitcnt lgkmcnt(3)
	v_mfma_f32_32x32x16_f16 v[114:129], v[134:137], v[162:165], v[114:129]
	v_mfma_f32_32x32x16_f16 v[34:49], v[134:137], v[166:169], v[34:49]
	ds_read_b128 v[134:137], v236 offset:39232
	s_waitcnt lgkmcnt(3)
	v_mfma_f32_32x32x16_f16 v[98:113], v[138:141], v[162:165], v[98:113]
	v_mfma_f32_32x32x16_f16 v[18:33], v[138:141], v[166:169], v[18:33]
	ds_read_b128 v[138:141], v236 offset:43584
	s_waitcnt lgkmcnt(3)
	v_mfma_f32_32x32x16_f16 v[66:81], v[142:145], v[162:165], v[66:81]
	v_mfma_f32_32x32x16_f16 v[2:17], v[142:145], v[166:169], v[2:17]
	ds_read_b128 v[142:145], v236 offset:47936
	global_load_dwordx4 v[162:165], v239, s[56:57]
	global_load_dwordx4 v[166:169], v239, s[56:57] offset:512
	s_add_u32 s56, s56, 0x4000
	s_addc_u32 s57, s57, 0
	s_waitcnt vmcnt(20)
	s_waitcnt lgkmcnt(3)
	v_mfma_f32_32x32x16_f16 v[82:97], v[130:133], v[170:173], v[82:97]
	v_mfma_f32_32x32x16_f16 v[50:65], v[130:133], v[174:177], v[50:65]
	ds_read_b128 v[130:133], v236 offset:34912
	s_waitcnt lgkmcnt(3)
	v_mfma_f32_32x32x16_f16 v[114:129], v[134:137], v[170:173], v[114:129]
	v_mfma_f32_32x32x16_f16 v[34:49], v[134:137], v[174:177], v[34:49]
	ds_read_b128 v[134:137], v236 offset:39264
	s_waitcnt lgkmcnt(3)
	v_mfma_f32_32x32x16_f16 v[98:113], v[138:141], v[170:173], v[98:113]
	v_mfma_f32_32x32x16_f16 v[18:33], v[138:141], v[174:177], v[18:33]
	ds_read_b128 v[138:141], v236 offset:43616
	s_waitcnt lgkmcnt(3)
	v_mfma_f32_32x32x16_f16 v[66:81], v[142:145], v[170:173], v[66:81]
	v_mfma_f32_32x32x16_f16 v[2:17], v[142:145], v[174:177], v[2:17]
	ds_read_b128 v[142:145], v236 offset:47968
	global_load_dwordx4 v[170:173], v239, s[56:57]
	global_load_dwordx4 v[174:177], v239, s[56:57] offset:512
	s_add_u32 s56, s56, 0x4000
	s_addc_u32 s57, s57, 0
	s_waitcnt vmcnt(20)
	s_waitcnt lgkmcnt(3)
	v_mfma_f32_32x32x16_f16 v[82:97], v[130:133], v[178:181], v[82:97]
	v_mfma_f32_32x32x16_f16 v[50:65], v[130:133], v[182:185], v[50:65]
	ds_read_b128 v[130:133], v236 offset:34944
	s_waitcnt lgkmcnt(3)
	v_mfma_f32_32x32x16_f16 v[114:129], v[134:137], v[178:181], v[114:129]
	v_mfma_f32_32x32x16_f16 v[34:49], v[134:137], v[182:185], v[34:49]
	ds_read_b128 v[134:137], v236 offset:39296
	s_waitcnt lgkmcnt(3)
	v_mfma_f32_32x32x16_f16 v[98:113], v[138:141], v[178:181], v[98:113]
	v_mfma_f32_32x32x16_f16 v[18:33], v[138:141], v[182:185], v[18:33]
	ds_read_b128 v[138:141], v236 offset:43648
	s_waitcnt lgkmcnt(3)
	v_mfma_f32_32x32x16_f16 v[66:81], v[142:145], v[178:181], v[66:81]
	v_mfma_f32_32x32x16_f16 v[2:17], v[142:145], v[182:185], v[2:17]
	ds_read_b128 v[142:145], v236 offset:48000
	global_load_dwordx4 v[178:181], v239, s[56:57]
	global_load_dwordx4 v[182:185], v239, s[56:57] offset:512
	s_add_u32 s56, s56, 0x4000
	s_addc_u32 s57, s57, 0
	s_waitcnt vmcnt(20)
	s_waitcnt lgkmcnt(3)
	v_mfma_f32_32x32x16_f16 v[82:97], v[130:133], v[186:189], v[82:97]
	v_mfma_f32_32x32x16_f16 v[50:65], v[130:133], v[190:193], v[50:65]
	ds_read_b128 v[130:133], v236 offset:34976
	s_waitcnt lgkmcnt(3)
	v_mfma_f32_32x32x16_f16 v[114:129], v[134:137], v[186:189], v[114:129]
	v_mfma_f32_32x32x16_f16 v[34:49], v[134:137], v[190:193], v[34:49]
	ds_read_b128 v[134:137], v236 offset:39328
	s_waitcnt lgkmcnt(3)
	v_mfma_f32_32x32x16_f16 v[98:113], v[138:141], v[186:189], v[98:113]
	v_mfma_f32_32x32x16_f16 v[18:33], v[138:141], v[190:193], v[18:33]
	ds_read_b128 v[138:141], v236 offset:43680
	s_waitcnt lgkmcnt(3)
	v_mfma_f32_32x32x16_f16 v[66:81], v[142:145], v[186:189], v[66:81]
	v_mfma_f32_32x32x16_f16 v[2:17], v[142:145], v[190:193], v[2:17]
	ds_read_b128 v[142:145], v236 offset:48032
	global_load_dwordx4 v[186:189], v239, s[56:57]
	global_load_dwordx4 v[190:193], v239, s[56:57] offset:512
	s_add_u32 s56, s56, 0x4000
	s_addc_u32 s57, s57, 0
	s_waitcnt vmcnt(12)
	s_waitcnt lgkmcnt(3)
	v_mfma_f32_32x32x16_f16 v[82:97], v[130:133], v[194:197], v[82:97]
	v_mfma_f32_32x32x16_f16 v[50:65], v[130:133], v[198:201], v[50:65]
	ds_read_b128 v[130:133], v236 offset:35008
	s_waitcnt lgkmcnt(3)
	v_mfma_f32_32x32x16_f16 v[114:129], v[134:137], v[194:197], v[114:129]
	v_mfma_f32_32x32x16_f16 v[34:49], v[134:137], v[198:201], v[34:49]
	ds_read_b128 v[134:137], v236 offset:39360
	s_waitcnt lgkmcnt(3)
	v_mfma_f32_32x32x16_f16 v[98:113], v[138:141], v[194:197], v[98:113]
	v_mfma_f32_32x32x16_f16 v[18:33], v[138:141], v[198:201], v[18:33]
	ds_read_b128 v[138:141], v236 offset:43712
	s_waitcnt lgkmcnt(3)
	v_mfma_f32_32x32x16_f16 v[66:81], v[142:145], v[194:197], v[66:81]
	v_mfma_f32_32x32x16_f16 v[2:17], v[142:145], v[198:201], v[2:17]
	ds_read_b128 v[142:145], v236 offset:48064
	global_load_dwordx4 v[194:197], v239, s[56:57]
	global_load_dwordx4 v[198:201], v239, s[56:57] offset:512
	s_add_u32 s56, s56, 0x4000
	s_addc_u32 s57, s57, 0
	s_waitcnt vmcnt(23)
	v_cvt_pk_f16_f32 v204, v204, v205
	v_cvt_pk_f16_f32 v205, v206, v207
	ds_write_b64 v237, v[204:205]
	s_waitcnt vmcnt(22)
	v_cvt_pk_f16_f32 v208, v208, v209
	v_cvt_pk_f16_f32 v209, v210, v211
	ds_write_b64 v237, v[208:209] offset:4352
	s_waitcnt vmcnt(21)
	v_cvt_pk_f16_f32 v212, v212, v213
	v_cvt_pk_f16_f32 v213, v214, v215
	ds_write_b64 v237, v[212:213] offset:8704
	s_waitcnt vmcnt(20)
	v_cvt_pk_f16_f32 v216, v216, v217
	v_cvt_pk_f16_f32 v217, v218, v219
	ds_write_b64 v237, v[216:217] offset:13056
	s_waitcnt vmcnt(19)
	v_cvt_pk_f16_f32 v220, v220, v221
	v_cvt_pk_f16_f32 v221, v222, v223
	ds_write_b64 v237, v[220:221] offset:17408
	s_waitcnt vmcnt(18)
	v_cvt_pk_f16_f32 v224, v224, v225
	v_cvt_pk_f16_f32 v225, v226, v227
	ds_write_b64 v237, v[224:225] offset:21760
	s_waitcnt vmcnt(17)
	v_cvt_pk_f16_f32 v228, v228, v229
	v_cvt_pk_f16_f32 v229, v230, v231
	ds_write_b64 v237, v[228:229] offset:26112
	s_waitcnt vmcnt(16)
	v_cvt_pk_f16_f32 v232, v232, v233
	v_cvt_pk_f16_f32 v233, v234, v235
	ds_write_b64 v237, v[232:233] offset:30464
	global_load_dwordx4 v[204:207], v238, s[40:41] offset:1536 nt
	global_load_dwordx4 v[208:211], v238, s[42:43] offset:1536 nt
	global_load_dwordx4 v[212:215], v238, s[44:45] offset:1536 nt
	global_load_dwordx4 v[216:219], v238, s[46:47] offset:1536 nt
	global_load_dwordx4 v[220:223], v238, s[48:49] offset:1536 nt
	global_load_dwordx4 v[224:227], v238, s[50:51] offset:1536 nt
	global_load_dwordx4 v[228:231], v238, s[52:53] offset:1536 nt
	global_load_dwordx4 v[232:235], v238, s[54:55] offset:1536 nt
	s_waitcnt vmcnt(20)
	s_waitcnt lgkmcnt(11)
	v_mfma_f32_32x32x16_f16 v[82:97], v[130:133], v[146:149], v[82:97]
	v_mfma_f32_32x32x16_f16 v[50:65], v[130:133], v[150:153], v[50:65]
	ds_read_b128 v[130:133], v236 offset:35040
	s_waitcnt lgkmcnt(11)
	v_mfma_f32_32x32x16_f16 v[114:129], v[134:137], v[146:149], v[114:129]
	v_mfma_f32_32x32x16_f16 v[34:49], v[134:137], v[150:153], v[34:49]
	ds_read_b128 v[134:137], v236 offset:39392
	s_waitcnt lgkmcnt(11)
	v_mfma_f32_32x32x16_f16 v[98:113], v[138:141], v[146:149], v[98:113]
	v_mfma_f32_32x32x16_f16 v[18:33], v[138:141], v[150:153], v[18:33]
	ds_read_b128 v[138:141], v236 offset:43744
	s_waitcnt lgkmcnt(11)
	v_mfma_f32_32x32x16_f16 v[66:81], v[142:145], v[146:149], v[66:81]
	v_mfma_f32_32x32x16_f16 v[2:17], v[142:145], v[150:153], v[2:17]
	ds_read_b128 v[142:145], v236 offset:48096
	global_load_dwordx4 v[146:149], v239, s[56:57]
	global_load_dwordx4 v[150:153], v239, s[56:57] offset:512
	s_add_u32 s56, s56, 0x4000
	s_addc_u32 s57, s57, 0
	s_waitcnt vmcnt(20)
	s_waitcnt lgkmcnt(3)
	v_mfma_f32_32x32x16_f16 v[82:97], v[130:133], v[154:157], v[82:97]
	v_mfma_f32_32x32x16_f16 v[50:65], v[130:133], v[158:161], v[50:65]
	s_waitcnt lgkmcnt(2)
	v_mfma_f32_32x32x16_f16 v[114:129], v[134:137], v[154:157], v[114:129]
	v_mfma_f32_32x32x16_f16 v[34:49], v[134:137], v[158:161], v[34:49]
	s_waitcnt lgkmcnt(1)
	v_mfma_f32_32x32x16_f16 v[98:113], v[138:141], v[154:157], v[98:113]
	v_mfma_f32_32x32x16_f16 v[18:33], v[138:141], v[158:161], v[18:33]
	s_waitcnt lgkmcnt(0)
	v_mfma_f32_32x32x16_f16 v[66:81], v[142:145], v[154:157], v[66:81]
	v_mfma_f32_32x32x16_f16 v[2:17], v[142:145], v[158:161], v[2:17]
	global_load_dwordx4 v[154:157], v239, s[56:57]
	global_load_dwordx4 v[158:161], v239, s[56:57] offset:512
	s_add_u32 s56, s56, 0x4000
	s_addc_u32 s57, s57, 0
	s_waitcnt lgkmcnt(0)
	s_barrier
	ds_read_b128 v[130:133], v236
	ds_read_b128 v[134:137], v236 offset:4352
	ds_read_b128 v[138:141], v236 offset:8704
	ds_read_b128 v[142:145], v236 offset:13056
	s_waitcnt vmcnt(20)
	s_waitcnt lgkmcnt(3)
	v_mfma_f32_32x32x16_f16 v[82:97], v[130:133], v[162:165], v[82:97]
	v_mfma_f32_32x32x16_f16 v[50:65], v[130:133], v[166:169], v[50:65]
	ds_read_b128 v[130:133], v236 offset:32
	s_waitcnt lgkmcnt(3)
	v_mfma_f32_32x32x16_f16 v[114:129], v[134:137], v[162:165], v[114:129]
	v_mfma_f32_32x32x16_f16 v[34:49], v[134:137], v[166:169], v[34:49]
	ds_read_b128 v[134:137], v236 offset:4384
	s_waitcnt lgkmcnt(3)
	v_mfma_f32_32x32x16_f16 v[98:113], v[138:141], v[162:165], v[98:113]
	v_mfma_f32_32x32x16_f16 v[18:33], v[138:141], v[166:169], v[18:33]
	ds_read_b128 v[138:141], v236 offset:8736
	s_waitcnt lgkmcnt(3)
	v_mfma_f32_32x32x16_f16 v[66:81], v[142:145], v[162:165], v[66:81]
	v_mfma_f32_32x32x16_f16 v[2:17], v[142:145], v[166:169], v[2:17]
	ds_read_b128 v[142:145], v236 offset:13088
	global_load_dwordx4 v[162:165], v239, s[56:57]
	global_load_dwordx4 v[166:169], v239, s[56:57] offset:512
	s_add_u32 s56, s56, 0x4000
	s_addc_u32 s57, s57, 0
	s_waitcnt vmcnt(20)
	s_waitcnt lgkmcnt(3)
	v_mfma_f32_32x32x16_f16 v[82:97], v[130:133], v[170:173], v[82:97]
	v_mfma_f32_32x32x16_f16 v[50:65], v[130:133], v[174:177], v[50:65]
	ds_read_b128 v[130:133], v236 offset:64
	s_waitcnt lgkmcnt(3)
	v_mfma_f32_32x32x16_f16 v[114:129], v[134:137], v[170:173], v[114:129]
	v_mfma_f32_32x32x16_f16 v[34:49], v[134:137], v[174:177], v[34:49]
	ds_read_b128 v[134:137], v236 offset:4416
	s_waitcnt lgkmcnt(3)
	v_mfma_f32_32x32x16_f16 v[98:113], v[138:141], v[170:173], v[98:113]
	v_mfma_f32_32x32x16_f16 v[18:33], v[138:141], v[174:177], v[18:33]
	ds_read_b128 v[138:141], v236 offset:8768
	s_waitcnt lgkmcnt(3)
	v_mfma_f32_32x32x16_f16 v[66:81], v[142:145], v[170:173], v[66:81]
	v_mfma_f32_32x32x16_f16 v[2:17], v[142:145], v[174:177], v[2:17]
	ds_read_b128 v[142:145], v236 offset:13120
	global_load_dwordx4 v[170:173], v239, s[56:57]
	global_load_dwordx4 v[174:177], v239, s[56:57] offset:512
	s_add_u32 s56, s56, 0x4000
	s_addc_u32 s57, s57, 0
	s_waitcnt vmcnt(20)
	s_waitcnt lgkmcnt(3)
	v_mfma_f32_32x32x16_f16 v[82:97], v[130:133], v[178:181], v[82:97]
	v_mfma_f32_32x32x16_f16 v[50:65], v[130:133], v[182:185], v[50:65]
	ds_read_b128 v[130:133], v236 offset:96
	s_waitcnt lgkmcnt(3)
	v_mfma_f32_32x32x16_f16 v[114:129], v[134:137], v[178:181], v[114:129]
	v_mfma_f32_32x32x16_f16 v[34:49], v[134:137], v[182:185], v[34:49]
	ds_read_b128 v[134:137], v236 offset:4448
	s_waitcnt lgkmcnt(3)
	v_mfma_f32_32x32x16_f16 v[98:113], v[138:141], v[178:181], v[98:113]
	v_mfma_f32_32x32x16_f16 v[18:33], v[138:141], v[182:185], v[18:33]
	ds_read_b128 v[138:141], v236 offset:8800
	s_waitcnt lgkmcnt(3)
	v_mfma_f32_32x32x16_f16 v[66:81], v[142:145], v[178:181], v[66:81]
	v_mfma_f32_32x32x16_f16 v[2:17], v[142:145], v[182:185], v[2:17]
	ds_read_b128 v[142:145], v236 offset:13152
	global_load_dwordx4 v[178:181], v239, s[56:57]
	global_load_dwordx4 v[182:185], v239, s[56:57] offset:512
	s_add_u32 s56, s56, 0x4000
	s_addc_u32 s57, s57, 0
	s_waitcnt vmcnt(20)
	s_waitcnt lgkmcnt(3)
	v_mfma_f32_32x32x16_f16 v[82:97], v[130:133], v[186:189], v[82:97]
	v_mfma_f32_32x32x16_f16 v[50:65], v[130:133], v[190:193], v[50:65]
	ds_read_b128 v[130:133], v236 offset:128
	s_waitcnt lgkmcnt(3)
	v_mfma_f32_32x32x16_f16 v[114:129], v[134:137], v[186:189], v[114:129]
	v_mfma_f32_32x32x16_f16 v[34:49], v[134:137], v[190:193], v[34:49]
	ds_read_b128 v[134:137], v236 offset:4480
	s_waitcnt lgkmcnt(3)
	v_mfma_f32_32x32x16_f16 v[98:113], v[138:141], v[186:189], v[98:113]
	v_mfma_f32_32x32x16_f16 v[18:33], v[138:141], v[190:193], v[18:33]
	ds_read_b128 v[138:141], v236 offset:8832
	s_waitcnt lgkmcnt(3)
	v_mfma_f32_32x32x16_f16 v[66:81], v[142:145], v[186:189], v[66:81]
	v_mfma_f32_32x32x16_f16 v[2:17], v[142:145], v[190:193], v[2:17]
	ds_read_b128 v[142:145], v236 offset:13184
	global_load_dwordx4 v[186:189], v239, s[56:57]
	global_load_dwordx4 v[190:193], v239, s[56:57] offset:512
	s_add_u32 s56, s56, 0x4000
	s_addc_u32 s57, s57, 0
	s_waitcnt vmcnt(20)
	s_waitcnt lgkmcnt(3)
	v_mfma_f32_32x32x16_f16 v[82:97], v[130:133], v[194:197], v[82:97]
	v_mfma_f32_32x32x16_f16 v[50:65], v[130:133], v[198:201], v[50:65]
	ds_read_b128 v[130:133], v236 offset:160
	s_waitcnt lgkmcnt(3)
	v_mfma_f32_32x32x16_f16 v[114:129], v[134:137], v[194:197], v[114:129]
	v_mfma_f32_32x32x16_f16 v[34:49], v[134:137], v[198:201], v[34:49]
	ds_read_b128 v[134:137], v236 offset:4512
	s_waitcnt lgkmcnt(3)
	v_mfma_f32_32x32x16_f16 v[98:113], v[138:141], v[194:197], v[98:113]
	v_mfma_f32_32x32x16_f16 v[18:33], v[138:141], v[198:201], v[18:33]
	ds_read_b128 v[138:141], v236 offset:8864
	s_waitcnt lgkmcnt(3)
	v_mfma_f32_32x32x16_f16 v[66:81], v[142:145], v[194:197], v[66:81]
	v_mfma_f32_32x32x16_f16 v[2:17], v[142:145], v[198:201], v[2:17]
	ds_read_b128 v[142:145], v236 offset:13216
	global_load_dwordx4 v[194:197], v239, s[56:57]
	global_load_dwordx4 v[198:201], v239, s[56:57] offset:512
	s_add_u32 s56, s56, 0x4000
	s_addc_u32 s57, s57, 0
	s_waitcnt vmcnt(12)
	s_waitcnt lgkmcnt(3)
	v_mfma_f32_32x32x16_f16 v[82:97], v[130:133], v[146:149], v[82:97]
	v_mfma_f32_32x32x16_f16 v[50:65], v[130:133], v[150:153], v[50:65]
	ds_read_b128 v[130:133], v236 offset:192
	s_waitcnt lgkmcnt(3)
	v_mfma_f32_32x32x16_f16 v[114:129], v[134:137], v[146:149], v[114:129]
	v_mfma_f32_32x32x16_f16 v[34:49], v[134:137], v[150:153], v[34:49]
	ds_read_b128 v[134:137], v236 offset:4544
	s_waitcnt lgkmcnt(3)
	v_mfma_f32_32x32x16_f16 v[98:113], v[138:141], v[146:149], v[98:113]
	v_mfma_f32_32x32x16_f16 v[18:33], v[138:141], v[150:153], v[18:33]
	ds_read_b128 v[138:141], v236 offset:8896
	s_waitcnt lgkmcnt(3)
	v_mfma_f32_32x32x16_f16 v[66:81], v[142:145], v[146:149], v[66:81]
	v_mfma_f32_32x32x16_f16 v[2:17], v[142:145], v[150:153], v[2:17]
	ds_read_b128 v[142:145], v236 offset:13248
	global_load_dwordx4 v[146:149], v239, s[56:57]
	global_load_dwordx4 v[150:153], v239, s[56:57] offset:512
	s_add_u32 s56, s56, 0x4000
	s_addc_u32 s57, s57, 0
	s_waitcnt vmcnt(23)
	v_cvt_pk_f16_f32 v204, v204, v205
	v_cvt_pk_f16_f32 v205, v206, v207
	ds_write_b64 v237, v[204:205] offset:34816
	s_waitcnt vmcnt(22)
	v_cvt_pk_f16_f32 v208, v208, v209
	v_cvt_pk_f16_f32 v209, v210, v211
	ds_write_b64 v237, v[208:209] offset:39168
	s_waitcnt vmcnt(21)
	v_cvt_pk_f16_f32 v212, v212, v213
	v_cvt_pk_f16_f32 v213, v214, v215
	ds_write_b64 v237, v[212:213] offset:43520
	s_waitcnt vmcnt(20)
	v_cvt_pk_f16_f32 v216, v216, v217
	v_cvt_pk_f16_f32 v217, v218, v219
	ds_write_b64 v237, v[216:217] offset:47872
	s_waitcnt vmcnt(19)
	v_cvt_pk_f16_f32 v220, v220, v221
	v_cvt_pk_f16_f32 v221, v222, v223
	ds_write_b64 v237, v[220:221] offset:52224
	s_waitcnt vmcnt(18)
	v_cvt_pk_f16_f32 v224, v224, v225
	v_cvt_pk_f16_f32 v225, v226, v227
	ds_write_b64 v237, v[224:225] offset:56576
	s_waitcnt vmcnt(17)
	v_cvt_pk_f16_f32 v228, v228, v229
	v_cvt_pk_f16_f32 v229, v230, v231
	ds_write_b64 v237, v[228:229] offset:60928
	s_waitcnt vmcnt(16)
	v_cvt_pk_f16_f32 v232, v232, v233
	v_cvt_pk_f16_f32 v233, v234, v235
	ds_write_b64 v237, v[232:233] offset:65280
	global_load_dwordx4 v[204:207], v238, s[40:41] offset:2048 nt
	global_load_dwordx4 v[208:211], v238, s[42:43] offset:2048 nt
	global_load_dwordx4 v[212:215], v238, s[44:45] offset:2048 nt
	global_load_dwordx4 v[216:219], v238, s[46:47] offset:2048 nt
	global_load_dwordx4 v[220:223], v238, s[48:49] offset:2048 nt
	global_load_dwordx4 v[224:227], v238, s[50:51] offset:2048 nt
	global_load_dwordx4 v[228:231], v238, s[52:53] offset:2048 nt
	global_load_dwordx4 v[232:235], v238, s[54:55] offset:2048 nt
	s_waitcnt vmcnt(20)
	s_waitcnt lgkmcnt(11)
	v_mfma_f32_32x32x16_f16 v[82:97], v[130:133], v[154:157], v[82:97]
	v_mfma_f32_32x32x16_f16 v[50:65], v[130:133], v[158:161], v[50:65]
	ds_read_b128 v[130:133], v236 offset:224
	s_waitcnt lgkmcnt(11)
	v_mfma_f32_32x32x16_f16 v[114:129], v[134:137], v[154:157], v[114:129]
	v_mfma_f32_32x32x16_f16 v[34:49], v[134:137], v[158:161], v[34:49]
	ds_read_b128 v[134:137], v236 offset:4576
	s_waitcnt lgkmcnt(11)
	v_mfma_f32_32x32x16_f16 v[98:113], v[138:141], v[154:157], v[98:113]
	v_mfma_f32_32x32x16_f16 v[18:33], v[138:141], v[158:161], v[18:33]
	ds_read_b128 v[138:141], v236 offset:8928
	s_waitcnt lgkmcnt(11)
	v_mfma_f32_32x32x16_f16 v[66:81], v[142:145], v[154:157], v[66:81]
	v_mfma_f32_32x32x16_f16 v[2:17], v[142:145], v[158:161], v[2:17]
	ds_read_b128 v[142:145], v236 offset:13280
	global_load_dwordx4 v[154:157], v239, s[56:57]
	global_load_dwordx4 v[158:161], v239, s[56:57] offset:512
	s_add_u32 s56, s56, 0x4000
	s_addc_u32 s57, s57, 0
	s_waitcnt vmcnt(20)
	s_waitcnt lgkmcnt(3)
	v_mfma_f32_32x32x16_f16 v[82:97], v[130:133], v[162:165], v[82:97]
	v_mfma_f32_32x32x16_f16 v[50:65], v[130:133], v[166:169], v[50:65]
	s_waitcnt lgkmcnt(2)
	v_mfma_f32_32x32x16_f16 v[114:129], v[134:137], v[162:165], v[114:129]
	v_mfma_f32_32x32x16_f16 v[34:49], v[134:137], v[166:169], v[34:49]
	s_waitcnt lgkmcnt(1)
	v_mfma_f32_32x32x16_f16 v[98:113], v[138:141], v[162:165], v[98:113]
	v_mfma_f32_32x32x16_f16 v[18:33], v[138:141], v[166:169], v[18:33]
	s_waitcnt lgkmcnt(0)
	v_mfma_f32_32x32x16_f16 v[66:81], v[142:145], v[162:165], v[66:81]
	v_mfma_f32_32x32x16_f16 v[2:17], v[142:145], v[166:169], v[2:17]
	global_load_dwordx4 v[162:165], v239, s[56:57]
	global_load_dwordx4 v[166:169], v239, s[56:57] offset:512
	s_add_u32 s56, s56, 0x4000
	s_addc_u32 s57, s57, 0
	s_waitcnt lgkmcnt(0)
	s_barrier
	ds_read_b128 v[130:133], v236 offset:34816
	ds_read_b128 v[134:137], v236 offset:39168
	ds_read_b128 v[138:141], v236 offset:43520
	ds_read_b128 v[142:145], v236 offset:47872
	s_waitcnt vmcnt(20)
	s_waitcnt lgkmcnt(3)
	v_mfma_f32_32x32x16_f16 v[82:97], v[130:133], v[170:173], v[82:97]
	v_mfma_f32_32x32x16_f16 v[50:65], v[130:133], v[174:177], v[50:65]
	ds_read_b128 v[130:133], v236 offset:34848
	s_waitcnt lgkmcnt(3)
	v_mfma_f32_32x32x16_f16 v[114:129], v[134:137], v[170:173], v[114:129]
	v_mfma_f32_32x32x16_f16 v[34:49], v[134:137], v[174:177], v[34:49]
	ds_read_b128 v[134:137], v236 offset:39200
	s_waitcnt lgkmcnt(3)
	v_mfma_f32_32x32x16_f16 v[98:113], v[138:141], v[170:173], v[98:113]
	v_mfma_f32_32x32x16_f16 v[18:33], v[138:141], v[174:177], v[18:33]
	ds_read_b128 v[138:141], v236 offset:43552
	s_waitcnt lgkmcnt(3)
	v_mfma_f32_32x32x16_f16 v[66:81], v[142:145], v[170:173], v[66:81]
	v_mfma_f32_32x32x16_f16 v[2:17], v[142:145], v[174:177], v[2:17]
	ds_read_b128 v[142:145], v236 offset:47904
	global_load_dwordx4 v[170:173], v239, s[56:57]
	global_load_dwordx4 v[174:177], v239, s[56:57] offset:512
	s_add_u32 s56, s56, 0x4000
	s_addc_u32 s57, s57, 0
	s_waitcnt vmcnt(20)
	s_waitcnt lgkmcnt(3)
	v_mfma_f32_32x32x16_f16 v[82:97], v[130:133], v[178:181], v[82:97]
	v_mfma_f32_32x32x16_f16 v[50:65], v[130:133], v[182:185], v[50:65]
	ds_read_b128 v[130:133], v236 offset:34880
	s_waitcnt lgkmcnt(3)
	v_mfma_f32_32x32x16_f16 v[114:129], v[134:137], v[178:181], v[114:129]
	v_mfma_f32_32x32x16_f16 v[34:49], v[134:137], v[182:185], v[34:49]
	ds_read_b128 v[134:137], v236 offset:39232
	s_waitcnt lgkmcnt(3)
	v_mfma_f32_32x32x16_f16 v[98:113], v[138:141], v[178:181], v[98:113]
	v_mfma_f32_32x32x16_f16 v[18:33], v[138:141], v[182:185], v[18:33]
	ds_read_b128 v[138:141], v236 offset:43584
	s_waitcnt lgkmcnt(3)
	v_mfma_f32_32x32x16_f16 v[66:81], v[142:145], v[178:181], v[66:81]
	v_mfma_f32_32x32x16_f16 v[2:17], v[142:145], v[182:185], v[2:17]
	ds_read_b128 v[142:145], v236 offset:47936
	global_load_dwordx4 v[178:181], v239, s[56:57]
	global_load_dwordx4 v[182:185], v239, s[56:57] offset:512
	s_add_u32 s56, s56, 0x4000
	s_addc_u32 s57, s57, 0
	s_waitcnt vmcnt(20)
	s_waitcnt lgkmcnt(3)
	v_mfma_f32_32x32x16_f16 v[82:97], v[130:133], v[186:189], v[82:97]
	v_mfma_f32_32x32x16_f16 v[50:65], v[130:133], v[190:193], v[50:65]
	ds_read_b128 v[130:133], v236 offset:34912
	s_waitcnt lgkmcnt(3)
	v_mfma_f32_32x32x16_f16 v[114:129], v[134:137], v[186:189], v[114:129]
	v_mfma_f32_32x32x16_f16 v[34:49], v[134:137], v[190:193], v[34:49]
	ds_read_b128 v[134:137], v236 offset:39264
	s_waitcnt lgkmcnt(3)
	v_mfma_f32_32x32x16_f16 v[98:113], v[138:141], v[186:189], v[98:113]
	v_mfma_f32_32x32x16_f16 v[18:33], v[138:141], v[190:193], v[18:33]
	ds_read_b128 v[138:141], v236 offset:43616
	s_waitcnt lgkmcnt(3)
	v_mfma_f32_32x32x16_f16 v[66:81], v[142:145], v[186:189], v[66:81]
	v_mfma_f32_32x32x16_f16 v[2:17], v[142:145], v[190:193], v[2:17]
	ds_read_b128 v[142:145], v236 offset:47968
	global_load_dwordx4 v[186:189], v239, s[56:57]
	global_load_dwordx4 v[190:193], v239, s[56:57] offset:512
	s_add_u32 s56, s56, 0x4000
	s_addc_u32 s57, s57, 0
	s_waitcnt vmcnt(20)
	s_waitcnt lgkmcnt(3)
	v_mfma_f32_32x32x16_f16 v[82:97], v[130:133], v[194:197], v[82:97]
	v_mfma_f32_32x32x16_f16 v[50:65], v[130:133], v[198:201], v[50:65]
	ds_read_b128 v[130:133], v236 offset:34944
	s_waitcnt lgkmcnt(3)
	v_mfma_f32_32x32x16_f16 v[114:129], v[134:137], v[194:197], v[114:129]
	v_mfma_f32_32x32x16_f16 v[34:49], v[134:137], v[198:201], v[34:49]
	ds_read_b128 v[134:137], v236 offset:39296
	s_waitcnt lgkmcnt(3)
	v_mfma_f32_32x32x16_f16 v[98:113], v[138:141], v[194:197], v[98:113]
	v_mfma_f32_32x32x16_f16 v[18:33], v[138:141], v[198:201], v[18:33]
	ds_read_b128 v[138:141], v236 offset:43648
	s_waitcnt lgkmcnt(3)
	v_mfma_f32_32x32x16_f16 v[66:81], v[142:145], v[194:197], v[66:81]
	v_mfma_f32_32x32x16_f16 v[2:17], v[142:145], v[198:201], v[2:17]
	ds_read_b128 v[142:145], v236 offset:48000
	global_load_dwordx4 v[194:197], v239, s[56:57]
	global_load_dwordx4 v[198:201], v239, s[56:57] offset:512
	s_add_u32 s56, s56, 0x4000
	s_addc_u32 s57, s57, 0
	s_waitcnt vmcnt(20)
	s_waitcnt lgkmcnt(3)
	v_mfma_f32_32x32x16_f16 v[82:97], v[130:133], v[146:149], v[82:97]
	v_mfma_f32_32x32x16_f16 v[50:65], v[130:133], v[150:153], v[50:65]
	ds_read_b128 v[130:133], v236 offset:34976
	s_waitcnt lgkmcnt(3)
	v_mfma_f32_32x32x16_f16 v[114:129], v[134:137], v[146:149], v[114:129]
	v_mfma_f32_32x32x16_f16 v[34:49], v[134:137], v[150:153], v[34:49]
	ds_read_b128 v[134:137], v236 offset:39328
	s_waitcnt lgkmcnt(3)
	v_mfma_f32_32x32x16_f16 v[98:113], v[138:141], v[146:149], v[98:113]
	v_mfma_f32_32x32x16_f16 v[18:33], v[138:141], v[150:153], v[18:33]
	ds_read_b128 v[138:141], v236 offset:43680
	s_waitcnt lgkmcnt(3)
	v_mfma_f32_32x32x16_f16 v[66:81], v[142:145], v[146:149], v[66:81]
	v_mfma_f32_32x32x16_f16 v[2:17], v[142:145], v[150:153], v[2:17]
	ds_read_b128 v[142:145], v236 offset:48032
	global_load_dwordx4 v[146:149], v239, s[56:57]
	global_load_dwordx4 v[150:153], v239, s[56:57] offset:512
	s_add_u32 s56, s56, 0x4000
	s_addc_u32 s57, s57, 0
	s_waitcnt vmcnt(12)
	s_waitcnt lgkmcnt(3)
	v_mfma_f32_32x32x16_f16 v[82:97], v[130:133], v[154:157], v[82:97]
	v_mfma_f32_32x32x16_f16 v[50:65], v[130:133], v[158:161], v[50:65]
	ds_read_b128 v[130:133], v236 offset:35008
	s_waitcnt lgkmcnt(3)
	v_mfma_f32_32x32x16_f16 v[114:129], v[134:137], v[154:157], v[114:129]
	v_mfma_f32_32x32x16_f16 v[34:49], v[134:137], v[158:161], v[34:49]
	ds_read_b128 v[134:137], v236 offset:39360
	s_waitcnt lgkmcnt(3)
	v_mfma_f32_32x32x16_f16 v[98:113], v[138:141], v[154:157], v[98:113]
	v_mfma_f32_32x32x16_f16 v[18:33], v[138:141], v[158:161], v[18:33]
	ds_read_b128 v[138:141], v236 offset:43712
	s_waitcnt lgkmcnt(3)
	v_mfma_f32_32x32x16_f16 v[66:81], v[142:145], v[154:157], v[66:81]
	v_mfma_f32_32x32x16_f16 v[2:17], v[142:145], v[158:161], v[2:17]
	ds_read_b128 v[142:145], v236 offset:48064
	global_load_dwordx4 v[154:157], v239, s[56:57]
	global_load_dwordx4 v[158:161], v239, s[56:57] offset:512
	s_add_u32 s56, s56, 0x4000
	s_addc_u32 s57, s57, 0
	s_waitcnt vmcnt(23)
	v_cvt_pk_f16_f32 v204, v204, v205
	v_cvt_pk_f16_f32 v205, v206, v207
	ds_write_b64 v237, v[204:205]
	s_waitcnt vmcnt(22)
	v_cvt_pk_f16_f32 v208, v208, v209
	v_cvt_pk_f16_f32 v209, v210, v211
	ds_write_b64 v237, v[208:209] offset:4352
	s_waitcnt vmcnt(21)
	v_cvt_pk_f16_f32 v212, v212, v213
	v_cvt_pk_f16_f32 v213, v214, v215
	ds_write_b64 v237, v[212:213] offset:8704
	s_waitcnt vmcnt(20)
	v_cvt_pk_f16_f32 v216, v216, v217
	v_cvt_pk_f16_f32 v217, v218, v219
	ds_write_b64 v237, v[216:217] offset:13056
	s_waitcnt vmcnt(19)
	v_cvt_pk_f16_f32 v220, v220, v221
	v_cvt_pk_f16_f32 v221, v222, v223
	ds_write_b64 v237, v[220:221] offset:17408
	s_waitcnt vmcnt(18)
	v_cvt_pk_f16_f32 v224, v224, v225
	v_cvt_pk_f16_f32 v225, v226, v227
	ds_write_b64 v237, v[224:225] offset:21760
	s_waitcnt vmcnt(17)
	v_cvt_pk_f16_f32 v228, v228, v229
	v_cvt_pk_f16_f32 v229, v230, v231
	ds_write_b64 v237, v[228:229] offset:26112
	s_waitcnt vmcnt(16)
	v_cvt_pk_f16_f32 v232, v232, v233
	v_cvt_pk_f16_f32 v233, v234, v235
	ds_write_b64 v237, v[232:233] offset:30464
	global_load_dwordx4 v[204:207], v238, s[40:41] offset:2560 nt
	global_load_dwordx4 v[208:211], v238, s[42:43] offset:2560 nt
	global_load_dwordx4 v[212:215], v238, s[44:45] offset:2560 nt
	global_load_dwordx4 v[216:219], v238, s[46:47] offset:2560 nt
	global_load_dwordx4 v[220:223], v238, s[48:49] offset:2560 nt
	global_load_dwordx4 v[224:227], v238, s[50:51] offset:2560 nt
	global_load_dwordx4 v[228:231], v238, s[52:53] offset:2560 nt
	global_load_dwordx4 v[232:235], v238, s[54:55] offset:2560 nt
	s_waitcnt vmcnt(20)
	s_waitcnt lgkmcnt(11)
	v_mfma_f32_32x32x16_f16 v[82:97], v[130:133], v[162:165], v[82:97]
	v_mfma_f32_32x32x16_f16 v[50:65], v[130:133], v[166:169], v[50:65]
	ds_read_b128 v[130:133], v236 offset:35040
	s_waitcnt lgkmcnt(11)
	v_mfma_f32_32x32x16_f16 v[114:129], v[134:137], v[162:165], v[114:129]
	v_mfma_f32_32x32x16_f16 v[34:49], v[134:137], v[166:169], v[34:49]
	ds_read_b128 v[134:137], v236 offset:39392
	s_waitcnt lgkmcnt(11)
	v_mfma_f32_32x32x16_f16 v[98:113], v[138:141], v[162:165], v[98:113]
	v_mfma_f32_32x32x16_f16 v[18:33], v[138:141], v[166:169], v[18:33]
	ds_read_b128 v[138:141], v236 offset:43744
	s_waitcnt lgkmcnt(11)
	v_mfma_f32_32x32x16_f16 v[66:81], v[142:145], v[162:165], v[66:81]
	v_mfma_f32_32x32x16_f16 v[2:17], v[142:145], v[166:169], v[2:17]
	ds_read_b128 v[142:145], v236 offset:48096
	global_load_dwordx4 v[162:165], v239, s[56:57]
	global_load_dwordx4 v[166:169], v239, s[56:57] offset:512
	s_add_u32 s56, s56, 0x4000
	s_addc_u32 s57, s57, 0
	s_waitcnt vmcnt(20)
	s_waitcnt lgkmcnt(3)
	v_mfma_f32_32x32x16_f16 v[82:97], v[130:133], v[170:173], v[82:97]
	v_mfma_f32_32x32x16_f16 v[50:65], v[130:133], v[174:177], v[50:65]
	s_waitcnt lgkmcnt(2)
	v_mfma_f32_32x32x16_f16 v[114:129], v[134:137], v[170:173], v[114:129]
	v_mfma_f32_32x32x16_f16 v[34:49], v[134:137], v[174:177], v[34:49]
	s_waitcnt lgkmcnt(1)
	v_mfma_f32_32x32x16_f16 v[98:113], v[138:141], v[170:173], v[98:113]
	v_mfma_f32_32x32x16_f16 v[18:33], v[138:141], v[174:177], v[18:33]
	s_waitcnt lgkmcnt(0)
	v_mfma_f32_32x32x16_f16 v[66:81], v[142:145], v[170:173], v[66:81]
	v_mfma_f32_32x32x16_f16 v[2:17], v[142:145], v[174:177], v[2:17]
	global_load_dwordx4 v[170:173], v239, s[56:57]
	global_load_dwordx4 v[174:177], v239, s[56:57] offset:512
	s_add_u32 s56, s56, 0x4000
	s_addc_u32 s57, s57, 0
	s_waitcnt lgkmcnt(0)
	s_barrier
	ds_read_b128 v[130:133], v236
	ds_read_b128 v[134:137], v236 offset:4352
	ds_read_b128 v[138:141], v236 offset:8704
	ds_read_b128 v[142:145], v236 offset:13056
	s_waitcnt vmcnt(20)
	s_waitcnt lgkmcnt(3)
	v_mfma_f32_32x32x16_f16 v[82:97], v[130:133], v[178:181], v[82:97]
	v_mfma_f32_32x32x16_f16 v[50:65], v[130:133], v[182:185], v[50:65]
	ds_read_b128 v[130:133], v236 offset:32
	s_waitcnt lgkmcnt(3)
	v_mfma_f32_32x32x16_f16 v[114:129], v[134:137], v[178:181], v[114:129]
	v_mfma_f32_32x32x16_f16 v[34:49], v[134:137], v[182:185], v[34:49]
	ds_read_b128 v[134:137], v236 offset:4384
	s_waitcnt lgkmcnt(3)
	v_mfma_f32_32x32x16_f16 v[98:113], v[138:141], v[178:181], v[98:113]
	v_mfma_f32_32x32x16_f16 v[18:33], v[138:141], v[182:185], v[18:33]
	ds_read_b128 v[138:141], v236 offset:8736
	s_waitcnt lgkmcnt(3)
	v_mfma_f32_32x32x16_f16 v[66:81], v[142:145], v[178:181], v[66:81]
	v_mfma_f32_32x32x16_f16 v[2:17], v[142:145], v[182:185], v[2:17]
	ds_read_b128 v[142:145], v236 offset:13088
	global_load_dwordx4 v[178:181], v239, s[56:57]
	global_load_dwordx4 v[182:185], v239, s[56:57] offset:512
	s_add_u32 s56, s56, 0x4000
	s_addc_u32 s57, s57, 0
	s_waitcnt vmcnt(20)
	s_waitcnt lgkmcnt(3)
	v_mfma_f32_32x32x16_f16 v[82:97], v[130:133], v[186:189], v[82:97]
	v_mfma_f32_32x32x16_f16 v[50:65], v[130:133], v[190:193], v[50:65]
	ds_read_b128 v[130:133], v236 offset:64
	s_waitcnt lgkmcnt(3)
	v_mfma_f32_32x32x16_f16 v[114:129], v[134:137], v[186:189], v[114:129]
	v_mfma_f32_32x32x16_f16 v[34:49], v[134:137], v[190:193], v[34:49]
	ds_read_b128 v[134:137], v236 offset:4416
	s_waitcnt lgkmcnt(3)
	v_mfma_f32_32x32x16_f16 v[98:113], v[138:141], v[186:189], v[98:113]
	v_mfma_f32_32x32x16_f16 v[18:33], v[138:141], v[190:193], v[18:33]
	ds_read_b128 v[138:141], v236 offset:8768
	s_waitcnt lgkmcnt(3)
	v_mfma_f32_32x32x16_f16 v[66:81], v[142:145], v[186:189], v[66:81]
	v_mfma_f32_32x32x16_f16 v[2:17], v[142:145], v[190:193], v[2:17]
	ds_read_b128 v[142:145], v236 offset:13120
	global_load_dwordx4 v[186:189], v239, s[56:57]
	global_load_dwordx4 v[190:193], v239, s[56:57] offset:512
	s_add_u32 s56, s56, 0x4000
	s_addc_u32 s57, s57, 0
	s_waitcnt vmcnt(20)
	s_waitcnt lgkmcnt(3)
	v_mfma_f32_32x32x16_f16 v[82:97], v[130:133], v[194:197], v[82:97]
	v_mfma_f32_32x32x16_f16 v[50:65], v[130:133], v[198:201], v[50:65]
	ds_read_b128 v[130:133], v236 offset:96
	s_waitcnt lgkmcnt(3)
	v_mfma_f32_32x32x16_f16 v[114:129], v[134:137], v[194:197], v[114:129]
	v_mfma_f32_32x32x16_f16 v[34:49], v[134:137], v[198:201], v[34:49]
	ds_read_b128 v[134:137], v236 offset:4448
	s_waitcnt lgkmcnt(3)
	v_mfma_f32_32x32x16_f16 v[98:113], v[138:141], v[194:197], v[98:113]
	v_mfma_f32_32x32x16_f16 v[18:33], v[138:141], v[198:201], v[18:33]
	ds_read_b128 v[138:141], v236 offset:8800
	s_waitcnt lgkmcnt(3)
	v_mfma_f32_32x32x16_f16 v[66:81], v[142:145], v[194:197], v[66:81]
	v_mfma_f32_32x32x16_f16 v[2:17], v[142:145], v[198:201], v[2:17]
	ds_read_b128 v[142:145], v236 offset:13152
	global_load_dwordx4 v[194:197], v239, s[56:57]
	global_load_dwordx4 v[198:201], v239, s[56:57] offset:512
	s_add_u32 s56, s56, 0x4000
	s_addc_u32 s57, s57, 0
	s_waitcnt vmcnt(20)
	s_waitcnt lgkmcnt(3)
	v_mfma_f32_32x32x16_f16 v[82:97], v[130:133], v[146:149], v[82:97]
	v_mfma_f32_32x32x16_f16 v[50:65], v[130:133], v[150:153], v[50:65]
	ds_read_b128 v[130:133], v236 offset:128
	s_waitcnt lgkmcnt(3)
	v_mfma_f32_32x32x16_f16 v[114:129], v[134:137], v[146:149], v[114:129]
	v_mfma_f32_32x32x16_f16 v[34:49], v[134:137], v[150:153], v[34:49]
	ds_read_b128 v[134:137], v236 offset:4480
	s_waitcnt lgkmcnt(3)
	v_mfma_f32_32x32x16_f16 v[98:113], v[138:141], v[146:149], v[98:113]
	v_mfma_f32_32x32x16_f16 v[18:33], v[138:141], v[150:153], v[18:33]
	ds_read_b128 v[138:141], v236 offset:8832
	s_waitcnt lgkmcnt(3)
	v_mfma_f32_32x32x16_f16 v[66:81], v[142:145], v[146:149], v[66:81]
	v_mfma_f32_32x32x16_f16 v[2:17], v[142:145], v[150:153], v[2:17]
	ds_read_b128 v[142:145], v236 offset:13184
	global_load_dwordx4 v[146:149], v239, s[56:57]
	global_load_dwordx4 v[150:153], v239, s[56:57] offset:512
	s_add_u32 s56, s56, 0x4000
	s_addc_u32 s57, s57, 0
	s_waitcnt vmcnt(20)
	s_waitcnt lgkmcnt(3)
	v_mfma_f32_32x32x16_f16 v[82:97], v[130:133], v[154:157], v[82:97]
	v_mfma_f32_32x32x16_f16 v[50:65], v[130:133], v[158:161], v[50:65]
	ds_read_b128 v[130:133], v236 offset:160
	s_waitcnt lgkmcnt(3)
	v_mfma_f32_32x32x16_f16 v[114:129], v[134:137], v[154:157], v[114:129]
	v_mfma_f32_32x32x16_f16 v[34:49], v[134:137], v[158:161], v[34:49]
	ds_read_b128 v[134:137], v236 offset:4512
	s_waitcnt lgkmcnt(3)
	v_mfma_f32_32x32x16_f16 v[98:113], v[138:141], v[154:157], v[98:113]
	v_mfma_f32_32x32x16_f16 v[18:33], v[138:141], v[158:161], v[18:33]
	ds_read_b128 v[138:141], v236 offset:8864
	s_waitcnt lgkmcnt(3)
	v_mfma_f32_32x32x16_f16 v[66:81], v[142:145], v[154:157], v[66:81]
	v_mfma_f32_32x32x16_f16 v[2:17], v[142:145], v[158:161], v[2:17]
	ds_read_b128 v[142:145], v236 offset:13216
	global_load_dwordx4 v[154:157], v239, s[56:57]
	global_load_dwordx4 v[158:161], v239, s[56:57] offset:512
	s_add_u32 s56, s56, 0x4000
	s_addc_u32 s57, s57, 0
	s_waitcnt vmcnt(12)
	s_waitcnt lgkmcnt(3)
	v_mfma_f32_32x32x16_f16 v[82:97], v[130:133], v[162:165], v[82:97]
	v_mfma_f32_32x32x16_f16 v[50:65], v[130:133], v[166:169], v[50:65]
	ds_read_b128 v[130:133], v236 offset:192
	s_waitcnt lgkmcnt(3)
	v_mfma_f32_32x32x16_f16 v[114:129], v[134:137], v[162:165], v[114:129]
	v_mfma_f32_32x32x16_f16 v[34:49], v[134:137], v[166:169], v[34:49]
	ds_read_b128 v[134:137], v236 offset:4544
	s_waitcnt lgkmcnt(3)
	v_mfma_f32_32x32x16_f16 v[98:113], v[138:141], v[162:165], v[98:113]
	v_mfma_f32_32x32x16_f16 v[18:33], v[138:141], v[166:169], v[18:33]
	ds_read_b128 v[138:141], v236 offset:8896
	s_waitcnt lgkmcnt(3)
	v_mfma_f32_32x32x16_f16 v[66:81], v[142:145], v[162:165], v[66:81]
	v_mfma_f32_32x32x16_f16 v[2:17], v[142:145], v[166:169], v[2:17]
	ds_read_b128 v[142:145], v236 offset:13248
	global_load_dwordx4 v[162:165], v239, s[56:57]
	global_load_dwordx4 v[166:169], v239, s[56:57] offset:512
	s_add_u32 s56, s56, 0x4000
	s_addc_u32 s57, s57, 0
	s_waitcnt vmcnt(23)
	v_cvt_pk_f16_f32 v204, v204, v205
	v_cvt_pk_f16_f32 v205, v206, v207
	ds_write_b64 v237, v[204:205] offset:34816
	s_waitcnt vmcnt(22)
	v_cvt_pk_f16_f32 v208, v208, v209
	v_cvt_pk_f16_f32 v209, v210, v211
	ds_write_b64 v237, v[208:209] offset:39168
	s_waitcnt vmcnt(21)
	v_cvt_pk_f16_f32 v212, v212, v213
	v_cvt_pk_f16_f32 v213, v214, v215
	ds_write_b64 v237, v[212:213] offset:43520
	s_waitcnt vmcnt(20)
	v_cvt_pk_f16_f32 v216, v216, v217
	v_cvt_pk_f16_f32 v217, v218, v219
	ds_write_b64 v237, v[216:217] offset:47872
	s_waitcnt vmcnt(19)
	v_cvt_pk_f16_f32 v220, v220, v221
	v_cvt_pk_f16_f32 v221, v222, v223
	ds_write_b64 v237, v[220:221] offset:52224
	s_waitcnt vmcnt(18)
	v_cvt_pk_f16_f32 v224, v224, v225
	v_cvt_pk_f16_f32 v225, v226, v227
	ds_write_b64 v237, v[224:225] offset:56576
	s_waitcnt vmcnt(17)
	v_cvt_pk_f16_f32 v228, v228, v229
	v_cvt_pk_f16_f32 v229, v230, v231
	ds_write_b64 v237, v[228:229] offset:60928
	s_waitcnt vmcnt(16)
	v_cvt_pk_f16_f32 v232, v232, v233
	v_cvt_pk_f16_f32 v233, v234, v235
	ds_write_b64 v237, v[232:233] offset:65280
	global_load_dwordx4 v[204:207], v238, s[40:41] offset:3072 nt
	global_load_dwordx4 v[208:211], v238, s[42:43] offset:3072 nt
	global_load_dwordx4 v[212:215], v238, s[44:45] offset:3072 nt
	global_load_dwordx4 v[216:219], v238, s[46:47] offset:3072 nt
	global_load_dwordx4 v[220:223], v238, s[48:49] offset:3072 nt
	global_load_dwordx4 v[224:227], v238, s[50:51] offset:3072 nt
	global_load_dwordx4 v[228:231], v238, s[52:53] offset:3072 nt
	global_load_dwordx4 v[232:235], v238, s[54:55] offset:3072 nt
	s_waitcnt vmcnt(20)
	s_waitcnt lgkmcnt(11)
	v_mfma_f32_32x32x16_f16 v[82:97], v[130:133], v[170:173], v[82:97]
	v_mfma_f32_32x32x16_f16 v[50:65], v[130:133], v[174:177], v[50:65]
	ds_read_b128 v[130:133], v236 offset:224
	s_waitcnt lgkmcnt(11)
	v_mfma_f32_32x32x16_f16 v[114:129], v[134:137], v[170:173], v[114:129]
	v_mfma_f32_32x32x16_f16 v[34:49], v[134:137], v[174:177], v[34:49]
	ds_read_b128 v[134:137], v236 offset:4576
	s_waitcnt lgkmcnt(11)
	v_mfma_f32_32x32x16_f16 v[98:113], v[138:141], v[170:173], v[98:113]
	v_mfma_f32_32x32x16_f16 v[18:33], v[138:141], v[174:177], v[18:33]
	ds_read_b128 v[138:141], v236 offset:8928
	s_waitcnt lgkmcnt(11)
	v_mfma_f32_32x32x16_f16 v[66:81], v[142:145], v[170:173], v[66:81]
	v_mfma_f32_32x32x16_f16 v[2:17], v[142:145], v[174:177], v[2:17]
	ds_read_b128 v[142:145], v236 offset:13280
	global_load_dwordx4 v[170:173], v239, s[56:57]
	global_load_dwordx4 v[174:177], v239, s[56:57] offset:512
	s_add_u32 s56, s56, 0x4000
	s_addc_u32 s57, s57, 0
	s_waitcnt vmcnt(20)
	s_waitcnt lgkmcnt(3)
	v_mfma_f32_32x32x16_f16 v[82:97], v[130:133], v[178:181], v[82:97]
	v_mfma_f32_32x32x16_f16 v[50:65], v[130:133], v[182:185], v[50:65]
	s_waitcnt lgkmcnt(2)
	v_mfma_f32_32x32x16_f16 v[114:129], v[134:137], v[178:181], v[114:129]
	v_mfma_f32_32x32x16_f16 v[34:49], v[134:137], v[182:185], v[34:49]
	s_waitcnt lgkmcnt(1)
	v_mfma_f32_32x32x16_f16 v[98:113], v[138:141], v[178:181], v[98:113]
	v_mfma_f32_32x32x16_f16 v[18:33], v[138:141], v[182:185], v[18:33]
	s_waitcnt lgkmcnt(0)
	v_mfma_f32_32x32x16_f16 v[66:81], v[142:145], v[178:181], v[66:81]
	v_mfma_f32_32x32x16_f16 v[2:17], v[142:145], v[182:185], v[2:17]
	global_load_dwordx4 v[178:181], v239, s[56:57]
	global_load_dwordx4 v[182:185], v239, s[56:57] offset:512
	s_add_u32 s56, s56, 0x4000
	s_addc_u32 s57, s57, 0
	s_waitcnt lgkmcnt(0)
	s_barrier
	ds_read_b128 v[130:133], v236 offset:34816
	ds_read_b128 v[134:137], v236 offset:39168
	ds_read_b128 v[138:141], v236 offset:43520
	ds_read_b128 v[142:145], v236 offset:47872
	s_waitcnt vmcnt(20)
	s_waitcnt lgkmcnt(3)
	v_mfma_f32_32x32x16_f16 v[82:97], v[130:133], v[186:189], v[82:97]
	v_mfma_f32_32x32x16_f16 v[50:65], v[130:133], v[190:193], v[50:65]
	ds_read_b128 v[130:133], v236 offset:34848
	s_waitcnt lgkmcnt(3)
	v_mfma_f32_32x32x16_f16 v[114:129], v[134:137], v[186:189], v[114:129]
	v_mfma_f32_32x32x16_f16 v[34:49], v[134:137], v[190:193], v[34:49]
	ds_read_b128 v[134:137], v236 offset:39200
	s_waitcnt lgkmcnt(3)
	v_mfma_f32_32x32x16_f16 v[98:113], v[138:141], v[186:189], v[98:113]
	v_mfma_f32_32x32x16_f16 v[18:33], v[138:141], v[190:193], v[18:33]
	ds_read_b128 v[138:141], v236 offset:43552
	s_waitcnt lgkmcnt(3)
	v_mfma_f32_32x32x16_f16 v[66:81], v[142:145], v[186:189], v[66:81]
	v_mfma_f32_32x32x16_f16 v[2:17], v[142:145], v[190:193], v[2:17]
	ds_read_b128 v[142:145], v236 offset:47904
	global_load_dwordx4 v[186:189], v239, s[56:57]
	global_load_dwordx4 v[190:193], v239, s[56:57] offset:512
	s_add_u32 s56, s56, 0x4000
	s_addc_u32 s57, s57, 0
	s_waitcnt vmcnt(20)
	s_waitcnt lgkmcnt(3)
	v_mfma_f32_32x32x16_f16 v[82:97], v[130:133], v[194:197], v[82:97]
	v_mfma_f32_32x32x16_f16 v[50:65], v[130:133], v[198:201], v[50:65]
	ds_read_b128 v[130:133], v236 offset:34880
	s_waitcnt lgkmcnt(3)
	v_mfma_f32_32x32x16_f16 v[114:129], v[134:137], v[194:197], v[114:129]
	v_mfma_f32_32x32x16_f16 v[34:49], v[134:137], v[198:201], v[34:49]
	ds_read_b128 v[134:137], v236 offset:39232
	s_waitcnt lgkmcnt(3)
	v_mfma_f32_32x32x16_f16 v[98:113], v[138:141], v[194:197], v[98:113]
	v_mfma_f32_32x32x16_f16 v[18:33], v[138:141], v[198:201], v[18:33]
	ds_read_b128 v[138:141], v236 offset:43584
	s_waitcnt lgkmcnt(3)
	v_mfma_f32_32x32x16_f16 v[66:81], v[142:145], v[194:197], v[66:81]
	v_mfma_f32_32x32x16_f16 v[2:17], v[142:145], v[198:201], v[2:17]
	ds_read_b128 v[142:145], v236 offset:47936
	global_load_dwordx4 v[194:197], v239, s[56:57]
	global_load_dwordx4 v[198:201], v239, s[56:57] offset:512
	s_add_u32 s56, s56, 0x4000
	s_addc_u32 s57, s57, 0
	s_waitcnt vmcnt(20)
	s_waitcnt lgkmcnt(3)
	v_mfma_f32_32x32x16_f16 v[82:97], v[130:133], v[146:149], v[82:97]
	v_mfma_f32_32x32x16_f16 v[50:65], v[130:133], v[150:153], v[50:65]
	ds_read_b128 v[130:133], v236 offset:34912
	s_waitcnt lgkmcnt(3)
	v_mfma_f32_32x32x16_f16 v[114:129], v[134:137], v[146:149], v[114:129]
	v_mfma_f32_32x32x16_f16 v[34:49], v[134:137], v[150:153], v[34:49]
	ds_read_b128 v[134:137], v236 offset:39264
	s_waitcnt lgkmcnt(3)
	v_mfma_f32_32x32x16_f16 v[98:113], v[138:141], v[146:149], v[98:113]
	v_mfma_f32_32x32x16_f16 v[18:33], v[138:141], v[150:153], v[18:33]
	ds_read_b128 v[138:141], v236 offset:43616
	s_waitcnt lgkmcnt(3)
	v_mfma_f32_32x32x16_f16 v[66:81], v[142:145], v[146:149], v[66:81]
	v_mfma_f32_32x32x16_f16 v[2:17], v[142:145], v[150:153], v[2:17]
	ds_read_b128 v[142:145], v236 offset:47968
	global_load_dwordx4 v[146:149], v239, s[56:57]
	global_load_dwordx4 v[150:153], v239, s[56:57] offset:512
	s_add_u32 s56, s56, 0x4000
	s_addc_u32 s57, s57, 0
	s_waitcnt vmcnt(20)
	s_waitcnt lgkmcnt(3)
	v_mfma_f32_32x32x16_f16 v[82:97], v[130:133], v[154:157], v[82:97]
	v_mfma_f32_32x32x16_f16 v[50:65], v[130:133], v[158:161], v[50:65]
	ds_read_b128 v[130:133], v236 offset:34944
	s_waitcnt lgkmcnt(3)
	v_mfma_f32_32x32x16_f16 v[114:129], v[134:137], v[154:157], v[114:129]
	v_mfma_f32_32x32x16_f16 v[34:49], v[134:137], v[158:161], v[34:49]
	ds_read_b128 v[134:137], v236 offset:39296
	s_waitcnt lgkmcnt(3)
	v_mfma_f32_32x32x16_f16 v[98:113], v[138:141], v[154:157], v[98:113]
	v_mfma_f32_32x32x16_f16 v[18:33], v[138:141], v[158:161], v[18:33]
	ds_read_b128 v[138:141], v236 offset:43648
	s_waitcnt lgkmcnt(3)
	v_mfma_f32_32x32x16_f16 v[66:81], v[142:145], v[154:157], v[66:81]
	v_mfma_f32_32x32x16_f16 v[2:17], v[142:145], v[158:161], v[2:17]
	ds_read_b128 v[142:145], v236 offset:48000
	global_load_dwordx4 v[154:157], v239, s[56:57]
	global_load_dwordx4 v[158:161], v239, s[56:57] offset:512
	s_add_u32 s56, s56, 0x4000
	s_addc_u32 s57, s57, 0
	s_waitcnt vmcnt(20)
	s_waitcnt lgkmcnt(3)
	v_mfma_f32_32x32x16_f16 v[82:97], v[130:133], v[162:165], v[82:97]
	v_mfma_f32_32x32x16_f16 v[50:65], v[130:133], v[166:169], v[50:65]
	ds_read_b128 v[130:133], v236 offset:34976
	s_waitcnt lgkmcnt(3)
	v_mfma_f32_32x32x16_f16 v[114:129], v[134:137], v[162:165], v[114:129]
	v_mfma_f32_32x32x16_f16 v[34:49], v[134:137], v[166:169], v[34:49]
	ds_read_b128 v[134:137], v236 offset:39328
	s_waitcnt lgkmcnt(3)
	v_mfma_f32_32x32x16_f16 v[98:113], v[138:141], v[162:165], v[98:113]
	v_mfma_f32_32x32x16_f16 v[18:33], v[138:141], v[166:169], v[18:33]
	ds_read_b128 v[138:141], v236 offset:43680
	s_waitcnt lgkmcnt(3)
	v_mfma_f32_32x32x16_f16 v[66:81], v[142:145], v[162:165], v[66:81]
	v_mfma_f32_32x32x16_f16 v[2:17], v[142:145], v[166:169], v[2:17]
	ds_read_b128 v[142:145], v236 offset:48032
	global_load_dwordx4 v[162:165], v239, s[56:57]
	global_load_dwordx4 v[166:169], v239, s[56:57] offset:512
	s_add_u32 s56, s56, 0x4000
	s_addc_u32 s57, s57, 0
	s_waitcnt vmcnt(12)
	s_waitcnt lgkmcnt(3)
	v_mfma_f32_32x32x16_f16 v[82:97], v[130:133], v[170:173], v[82:97]
	v_mfma_f32_32x32x16_f16 v[50:65], v[130:133], v[174:177], v[50:65]
	ds_read_b128 v[130:133], v236 offset:35008
	s_waitcnt lgkmcnt(3)
	v_mfma_f32_32x32x16_f16 v[114:129], v[134:137], v[170:173], v[114:129]
	v_mfma_f32_32x32x16_f16 v[34:49], v[134:137], v[174:177], v[34:49]
	ds_read_b128 v[134:137], v236 offset:39360
	s_waitcnt lgkmcnt(3)
	v_mfma_f32_32x32x16_f16 v[98:113], v[138:141], v[170:173], v[98:113]
	v_mfma_f32_32x32x16_f16 v[18:33], v[138:141], v[174:177], v[18:33]
	ds_read_b128 v[138:141], v236 offset:43712
	s_waitcnt lgkmcnt(3)
	v_mfma_f32_32x32x16_f16 v[66:81], v[142:145], v[170:173], v[66:81]
	v_mfma_f32_32x32x16_f16 v[2:17], v[142:145], v[174:177], v[2:17]
	ds_read_b128 v[142:145], v236 offset:48064
	global_load_dwordx4 v[170:173], v239, s[56:57]
	global_load_dwordx4 v[174:177], v239, s[56:57] offset:512
	s_add_u32 s56, s56, 0x4000
	s_addc_u32 s57, s57, 0
	s_waitcnt vmcnt(23)
	v_cvt_pk_f16_f32 v204, v204, v205
	v_cvt_pk_f16_f32 v205, v206, v207
	ds_write_b64 v237, v[204:205]
	s_waitcnt vmcnt(22)
	v_cvt_pk_f16_f32 v208, v208, v209
	v_cvt_pk_f16_f32 v209, v210, v211
	ds_write_b64 v237, v[208:209] offset:4352
	s_waitcnt vmcnt(21)
	v_cvt_pk_f16_f32 v212, v212, v213
	v_cvt_pk_f16_f32 v213, v214, v215
	ds_write_b64 v237, v[212:213] offset:8704
	s_waitcnt vmcnt(20)
	v_cvt_pk_f16_f32 v216, v216, v217
	v_cvt_pk_f16_f32 v217, v218, v219
	ds_write_b64 v237, v[216:217] offset:13056
	s_waitcnt vmcnt(19)
	v_cvt_pk_f16_f32 v220, v220, v221
	v_cvt_pk_f16_f32 v221, v222, v223
	ds_write_b64 v237, v[220:221] offset:17408
	s_waitcnt vmcnt(18)
	v_cvt_pk_f16_f32 v224, v224, v225
	v_cvt_pk_f16_f32 v225, v226, v227
	ds_write_b64 v237, v[224:225] offset:21760
	s_waitcnt vmcnt(17)
	v_cvt_pk_f16_f32 v228, v228, v229
	v_cvt_pk_f16_f32 v229, v230, v231
	ds_write_b64 v237, v[228:229] offset:26112
	s_waitcnt vmcnt(16)
	v_cvt_pk_f16_f32 v232, v232, v233
	v_cvt_pk_f16_f32 v233, v234, v235
	ds_write_b64 v237, v[232:233] offset:30464
	global_load_dwordx4 v[204:207], v238, s[40:41] offset:3584 nt
	global_load_dwordx4 v[208:211], v238, s[42:43] offset:3584 nt
	global_load_dwordx4 v[212:215], v238, s[44:45] offset:3584 nt
	global_load_dwordx4 v[216:219], v238, s[46:47] offset:3584 nt
	global_load_dwordx4 v[220:223], v238, s[48:49] offset:3584 nt
	global_load_dwordx4 v[224:227], v238, s[50:51] offset:3584 nt
	global_load_dwordx4 v[228:231], v238, s[52:53] offset:3584 nt
	global_load_dwordx4 v[232:235], v238, s[54:55] offset:3584 nt
	s_waitcnt vmcnt(20)
	s_waitcnt lgkmcnt(11)
	v_mfma_f32_32x32x16_f16 v[82:97], v[130:133], v[178:181], v[82:97]
	v_mfma_f32_32x32x16_f16 v[50:65], v[130:133], v[182:185], v[50:65]
	ds_read_b128 v[130:133], v236 offset:35040
	s_waitcnt lgkmcnt(11)
	v_mfma_f32_32x32x16_f16 v[114:129], v[134:137], v[178:181], v[114:129]
	v_mfma_f32_32x32x16_f16 v[34:49], v[134:137], v[182:185], v[34:49]
	ds_read_b128 v[134:137], v236 offset:39392
	s_waitcnt lgkmcnt(11)
	v_mfma_f32_32x32x16_f16 v[98:113], v[138:141], v[178:181], v[98:113]
	v_mfma_f32_32x32x16_f16 v[18:33], v[138:141], v[182:185], v[18:33]
	ds_read_b128 v[138:141], v236 offset:43744
	s_waitcnt lgkmcnt(11)
	v_mfma_f32_32x32x16_f16 v[66:81], v[142:145], v[178:181], v[66:81]
	v_mfma_f32_32x32x16_f16 v[2:17], v[142:145], v[182:185], v[2:17]
	ds_read_b128 v[142:145], v236 offset:48096
	global_load_dwordx4 v[178:181], v239, s[56:57]
	global_load_dwordx4 v[182:185], v239, s[56:57] offset:512
	s_add_u32 s56, s56, 0x4000
	s_addc_u32 s57, s57, 0
	s_waitcnt vmcnt(20)
	s_waitcnt lgkmcnt(3)
	v_mfma_f32_32x32x16_f16 v[82:97], v[130:133], v[186:189], v[82:97]
	v_mfma_f32_32x32x16_f16 v[50:65], v[130:133], v[190:193], v[50:65]
	s_waitcnt lgkmcnt(2)
	v_mfma_f32_32x32x16_f16 v[114:129], v[134:137], v[186:189], v[114:129]
	v_mfma_f32_32x32x16_f16 v[34:49], v[134:137], v[190:193], v[34:49]
	s_waitcnt lgkmcnt(1)
	v_mfma_f32_32x32x16_f16 v[98:113], v[138:141], v[186:189], v[98:113]
	v_mfma_f32_32x32x16_f16 v[18:33], v[138:141], v[190:193], v[18:33]
	s_waitcnt lgkmcnt(0)
	v_mfma_f32_32x32x16_f16 v[66:81], v[142:145], v[186:189], v[66:81]
	v_mfma_f32_32x32x16_f16 v[2:17], v[142:145], v[190:193], v[2:17]
	global_load_dwordx4 v[186:189], v239, s[56:57]
	global_load_dwordx4 v[190:193], v239, s[56:57] offset:512
	s_add_u32 s56, s56, 0x4000
	s_addc_u32 s57, s57, 0
	s_waitcnt lgkmcnt(0)
	s_barrier
	ds_read_b128 v[130:133], v236
	ds_read_b128 v[134:137], v236 offset:4352
	ds_read_b128 v[138:141], v236 offset:8704
	ds_read_b128 v[142:145], v236 offset:13056
	s_waitcnt vmcnt(20)
	s_waitcnt lgkmcnt(3)
	v_mfma_f32_32x32x16_f16 v[82:97], v[130:133], v[194:197], v[82:97]
	v_mfma_f32_32x32x16_f16 v[50:65], v[130:133], v[198:201], v[50:65]
	ds_read_b128 v[130:133], v236 offset:32
	s_waitcnt lgkmcnt(3)
	v_mfma_f32_32x32x16_f16 v[114:129], v[134:137], v[194:197], v[114:129]
	v_mfma_f32_32x32x16_f16 v[34:49], v[134:137], v[198:201], v[34:49]
	ds_read_b128 v[134:137], v236 offset:4384
	s_waitcnt lgkmcnt(3)
	v_mfma_f32_32x32x16_f16 v[98:113], v[138:141], v[194:197], v[98:113]
	v_mfma_f32_32x32x16_f16 v[18:33], v[138:141], v[198:201], v[18:33]
	ds_read_b128 v[138:141], v236 offset:8736
	s_waitcnt lgkmcnt(3)
	v_mfma_f32_32x32x16_f16 v[66:81], v[142:145], v[194:197], v[66:81]
	v_mfma_f32_32x32x16_f16 v[2:17], v[142:145], v[198:201], v[2:17]
	ds_read_b128 v[142:145], v236 offset:13088
	global_load_dwordx4 v[194:197], v239, s[56:57]
	global_load_dwordx4 v[198:201], v239, s[56:57] offset:512
	s_add_u32 s56, s56, 0x4000
	s_addc_u32 s57, s57, 0
	s_waitcnt vmcnt(20)
	s_waitcnt lgkmcnt(3)
	v_mfma_f32_32x32x16_f16 v[82:97], v[130:133], v[146:149], v[82:97]
	v_mfma_f32_32x32x16_f16 v[50:65], v[130:133], v[150:153], v[50:65]
	ds_read_b128 v[130:133], v236 offset:64
	s_waitcnt lgkmcnt(3)
	v_mfma_f32_32x32x16_f16 v[114:129], v[134:137], v[146:149], v[114:129]
	v_mfma_f32_32x32x16_f16 v[34:49], v[134:137], v[150:153], v[34:49]
	ds_read_b128 v[134:137], v236 offset:4416
	s_waitcnt lgkmcnt(3)
	v_mfma_f32_32x32x16_f16 v[98:113], v[138:141], v[146:149], v[98:113]
	v_mfma_f32_32x32x16_f16 v[18:33], v[138:141], v[150:153], v[18:33]
	ds_read_b128 v[138:141], v236 offset:8768
	s_waitcnt lgkmcnt(3)
	v_mfma_f32_32x32x16_f16 v[66:81], v[142:145], v[146:149], v[66:81]
	v_mfma_f32_32x32x16_f16 v[2:17], v[142:145], v[150:153], v[2:17]
	ds_read_b128 v[142:145], v236 offset:13120
	global_load_dwordx4 v[146:149], v239, s[56:57]
	global_load_dwordx4 v[150:153], v239, s[56:57] offset:512
	s_add_u32 s56, s56, 0x4000
	s_addc_u32 s57, s57, 0
	s_waitcnt vmcnt(20)
	s_waitcnt lgkmcnt(3)
	v_mfma_f32_32x32x16_f16 v[82:97], v[130:133], v[154:157], v[82:97]
	v_mfma_f32_32x32x16_f16 v[50:65], v[130:133], v[158:161], v[50:65]
	ds_read_b128 v[130:133], v236 offset:96
	s_waitcnt lgkmcnt(3)
	v_mfma_f32_32x32x16_f16 v[114:129], v[134:137], v[154:157], v[114:129]
	v_mfma_f32_32x32x16_f16 v[34:49], v[134:137], v[158:161], v[34:49]
	ds_read_b128 v[134:137], v236 offset:4448
	s_waitcnt lgkmcnt(3)
	v_mfma_f32_32x32x16_f16 v[98:113], v[138:141], v[154:157], v[98:113]
	v_mfma_f32_32x32x16_f16 v[18:33], v[138:141], v[158:161], v[18:33]
	ds_read_b128 v[138:141], v236 offset:8800
	s_waitcnt lgkmcnt(3)
	v_mfma_f32_32x32x16_f16 v[66:81], v[142:145], v[154:157], v[66:81]
	v_mfma_f32_32x32x16_f16 v[2:17], v[142:145], v[158:161], v[2:17]
	ds_read_b128 v[142:145], v236 offset:13152
	global_load_dwordx4 v[154:157], v239, s[56:57]
	global_load_dwordx4 v[158:161], v239, s[56:57] offset:512
	s_add_u32 s56, s56, 0x4000
	s_addc_u32 s57, s57, 0
	s_waitcnt vmcnt(20)
	s_waitcnt lgkmcnt(3)
	v_mfma_f32_32x32x16_f16 v[82:97], v[130:133], v[162:165], v[82:97]
	v_mfma_f32_32x32x16_f16 v[50:65], v[130:133], v[166:169], v[50:65]
	ds_read_b128 v[130:133], v236 offset:128
	s_waitcnt lgkmcnt(3)
	v_mfma_f32_32x32x16_f16 v[114:129], v[134:137], v[162:165], v[114:129]
	v_mfma_f32_32x32x16_f16 v[34:49], v[134:137], v[166:169], v[34:49]
	ds_read_b128 v[134:137], v236 offset:4480
	s_waitcnt lgkmcnt(3)
	v_mfma_f32_32x32x16_f16 v[98:113], v[138:141], v[162:165], v[98:113]
	v_mfma_f32_32x32x16_f16 v[18:33], v[138:141], v[166:169], v[18:33]
	ds_read_b128 v[138:141], v236 offset:8832
	s_waitcnt lgkmcnt(3)
	v_mfma_f32_32x32x16_f16 v[66:81], v[142:145], v[162:165], v[66:81]
	v_mfma_f32_32x32x16_f16 v[2:17], v[142:145], v[166:169], v[2:17]
	ds_read_b128 v[142:145], v236 offset:13184
	global_load_dwordx4 v[162:165], v239, s[56:57]
	global_load_dwordx4 v[166:169], v239, s[56:57] offset:512
	s_add_u32 s56, s56, 0x4000
	s_addc_u32 s57, s57, 0
	s_waitcnt vmcnt(20)
	s_waitcnt lgkmcnt(3)
	v_mfma_f32_32x32x16_f16 v[82:97], v[130:133], v[170:173], v[82:97]
	v_mfma_f32_32x32x16_f16 v[50:65], v[130:133], v[174:177], v[50:65]
	ds_read_b128 v[130:133], v236 offset:160
	s_waitcnt lgkmcnt(3)
	v_mfma_f32_32x32x16_f16 v[114:129], v[134:137], v[170:173], v[114:129]
	v_mfma_f32_32x32x16_f16 v[34:49], v[134:137], v[174:177], v[34:49]
	ds_read_b128 v[134:137], v236 offset:4512
	s_waitcnt lgkmcnt(3)
	v_mfma_f32_32x32x16_f16 v[98:113], v[138:141], v[170:173], v[98:113]
	v_mfma_f32_32x32x16_f16 v[18:33], v[138:141], v[174:177], v[18:33]
	ds_read_b128 v[138:141], v236 offset:8864
	s_waitcnt lgkmcnt(3)
	v_mfma_f32_32x32x16_f16 v[66:81], v[142:145], v[170:173], v[66:81]
	v_mfma_f32_32x32x16_f16 v[2:17], v[142:145], v[174:177], v[2:17]
	ds_read_b128 v[142:145], v236 offset:13216
	global_load_dwordx4 v[170:173], v239, s[56:57]
	global_load_dwordx4 v[174:177], v239, s[56:57] offset:512
	s_add_u32 s56, s56, 0x4000
	s_addc_u32 s57, s57, 0
	s_waitcnt vmcnt(12)
	s_waitcnt lgkmcnt(3)
	v_mfma_f32_32x32x16_f16 v[82:97], v[130:133], v[178:181], v[82:97]
	v_mfma_f32_32x32x16_f16 v[50:65], v[130:133], v[182:185], v[50:65]
	ds_read_b128 v[130:133], v236 offset:192
	s_waitcnt lgkmcnt(3)
	v_mfma_f32_32x32x16_f16 v[114:129], v[134:137], v[178:181], v[114:129]
	v_mfma_f32_32x32x16_f16 v[34:49], v[134:137], v[182:185], v[34:49]
	ds_read_b128 v[134:137], v236 offset:4544
	s_waitcnt lgkmcnt(3)
	v_mfma_f32_32x32x16_f16 v[98:113], v[138:141], v[178:181], v[98:113]
	v_mfma_f32_32x32x16_f16 v[18:33], v[138:141], v[182:185], v[18:33]
	ds_read_b128 v[138:141], v236 offset:8896
	s_waitcnt lgkmcnt(3)
	v_mfma_f32_32x32x16_f16 v[66:81], v[142:145], v[178:181], v[66:81]
	v_mfma_f32_32x32x16_f16 v[2:17], v[142:145], v[182:185], v[2:17]
	ds_read_b128 v[142:145], v236 offset:13248
	global_load_dwordx4 v[178:181], v239, s[56:57]
	global_load_dwordx4 v[182:185], v239, s[56:57] offset:512
	s_add_u32 s56, s56, 0x4000
	s_addc_u32 s57, s57, 0
	s_waitcnt vmcnt(23)
	v_cvt_pk_f16_f32 v204, v204, v205
	v_cvt_pk_f16_f32 v205, v206, v207
	ds_write_b64 v237, v[204:205] offset:34816
	s_waitcnt vmcnt(22)
	v_cvt_pk_f16_f32 v208, v208, v209
	v_cvt_pk_f16_f32 v209, v210, v211
	ds_write_b64 v237, v[208:209] offset:39168
	s_waitcnt vmcnt(21)
	v_cvt_pk_f16_f32 v212, v212, v213
	v_cvt_pk_f16_f32 v213, v214, v215
	ds_write_b64 v237, v[212:213] offset:43520
	s_waitcnt vmcnt(20)
	v_cvt_pk_f16_f32 v216, v216, v217
	v_cvt_pk_f16_f32 v217, v218, v219
	ds_write_b64 v237, v[216:217] offset:47872
	s_waitcnt vmcnt(19)
	v_cvt_pk_f16_f32 v220, v220, v221
	v_cvt_pk_f16_f32 v221, v222, v223
	ds_write_b64 v237, v[220:221] offset:52224
	s_waitcnt vmcnt(18)
	v_cvt_pk_f16_f32 v224, v224, v225
	v_cvt_pk_f16_f32 v225, v226, v227
	ds_write_b64 v237, v[224:225] offset:56576
	s_waitcnt vmcnt(17)
	v_cvt_pk_f16_f32 v228, v228, v229
	v_cvt_pk_f16_f32 v229, v230, v231
	ds_write_b64 v237, v[228:229] offset:60928
	s_waitcnt vmcnt(16)
	v_cvt_pk_f16_f32 v232, v232, v233
	v_cvt_pk_f16_f32 v233, v234, v235
	ds_write_b64 v237, v[232:233] offset:65280
	s_waitcnt vmcnt(12)
	s_waitcnt lgkmcnt(11)
	v_mfma_f32_32x32x16_f16 v[82:97], v[130:133], v[186:189], v[82:97]
	v_mfma_f32_32x32x16_f16 v[50:65], v[130:133], v[190:193], v[50:65]
	ds_read_b128 v[130:133], v236 offset:224
	s_waitcnt lgkmcnt(11)
	v_mfma_f32_32x32x16_f16 v[114:129], v[134:137], v[186:189], v[114:129]
	v_mfma_f32_32x32x16_f16 v[34:49], v[134:137], v[190:193], v[34:49]
	ds_read_b128 v[134:137], v236 offset:4576
	s_waitcnt lgkmcnt(11)
	v_mfma_f32_32x32x16_f16 v[98:113], v[138:141], v[186:189], v[98:113]
	v_mfma_f32_32x32x16_f16 v[18:33], v[138:141], v[190:193], v[18:33]
	ds_read_b128 v[138:141], v236 offset:8928
	s_waitcnt lgkmcnt(11)
	v_mfma_f32_32x32x16_f16 v[66:81], v[142:145], v[186:189], v[66:81]
	v_mfma_f32_32x32x16_f16 v[2:17], v[142:145], v[190:193], v[2:17]
	ds_read_b128 v[142:145], v236 offset:13280
	global_load_dwordx4 v[186:189], v239, s[56:57]
	global_load_dwordx4 v[190:193], v239, s[56:57] offset:512
	s_add_u32 s56, s56, 0x4000
	s_addc_u32 s57, s57, 0
	s_waitcnt vmcnt(12)
	s_waitcnt lgkmcnt(3)
	v_mfma_f32_32x32x16_f16 v[82:97], v[130:133], v[194:197], v[82:97]
	v_mfma_f32_32x32x16_f16 v[50:65], v[130:133], v[198:201], v[50:65]
	s_waitcnt lgkmcnt(2)
	v_mfma_f32_32x32x16_f16 v[114:129], v[134:137], v[194:197], v[114:129]
	v_mfma_f32_32x32x16_f16 v[34:49], v[134:137], v[198:201], v[34:49]
	s_waitcnt lgkmcnt(1)
	v_mfma_f32_32x32x16_f16 v[98:113], v[138:141], v[194:197], v[98:113]
	v_mfma_f32_32x32x16_f16 v[18:33], v[138:141], v[198:201], v[18:33]
	s_waitcnt lgkmcnt(0)
	v_mfma_f32_32x32x16_f16 v[66:81], v[142:145], v[194:197], v[66:81]
	v_mfma_f32_32x32x16_f16 v[2:17], v[142:145], v[198:201], v[2:17]
	global_load_dwordx4 v[194:197], v239, s[56:57]
	global_load_dwordx4 v[198:201], v239, s[56:57] offset:512
	s_add_u32 s56, s56, 0x4000
	s_addc_u32 s57, s57, 0
	s_waitcnt lgkmcnt(0)
	s_barrier
	ds_read_b128 v[130:133], v236 offset:34816
	ds_read_b128 v[134:137], v236 offset:39168
	ds_read_b128 v[138:141], v236 offset:43520
	ds_read_b128 v[142:145], v236 offset:47872
	s_waitcnt vmcnt(12)
	s_waitcnt lgkmcnt(3)
	v_mfma_f32_32x32x16_f16 v[82:97], v[130:133], v[146:149], v[82:97]
	v_mfma_f32_32x32x16_f16 v[50:65], v[130:133], v[150:153], v[50:65]
	ds_read_b128 v[130:133], v236 offset:34848
	s_waitcnt lgkmcnt(3)
	v_mfma_f32_32x32x16_f16 v[114:129], v[134:137], v[146:149], v[114:129]
	v_mfma_f32_32x32x16_f16 v[34:49], v[134:137], v[150:153], v[34:49]
	ds_read_b128 v[134:137], v236 offset:39200
	s_waitcnt lgkmcnt(3)
	v_mfma_f32_32x32x16_f16 v[98:113], v[138:141], v[146:149], v[98:113]
	v_mfma_f32_32x32x16_f16 v[18:33], v[138:141], v[150:153], v[18:33]
	ds_read_b128 v[138:141], v236 offset:43552
	s_waitcnt lgkmcnt(3)
	v_mfma_f32_32x32x16_f16 v[66:81], v[142:145], v[146:149], v[66:81]
	v_mfma_f32_32x32x16_f16 v[2:17], v[142:145], v[150:153], v[2:17]
	ds_read_b128 v[142:145], v236 offset:47904
	global_load_dwordx4 v[146:149], v239, s[56:57]
	global_load_dwordx4 v[150:153], v239, s[56:57] offset:512
	s_add_u32 s56, s56, 0x4000
	s_addc_u32 s57, s57, 0
	s_waitcnt vmcnt(12)
	s_waitcnt lgkmcnt(3)
	v_mfma_f32_32x32x16_f16 v[82:97], v[130:133], v[154:157], v[82:97]
	v_mfma_f32_32x32x16_f16 v[50:65], v[130:133], v[158:161], v[50:65]
	ds_read_b128 v[130:133], v236 offset:34880
	s_waitcnt lgkmcnt(3)
	v_mfma_f32_32x32x16_f16 v[114:129], v[134:137], v[154:157], v[114:129]
	v_mfma_f32_32x32x16_f16 v[34:49], v[134:137], v[158:161], v[34:49]
	ds_read_b128 v[134:137], v236 offset:39232
	s_waitcnt lgkmcnt(3)
	v_mfma_f32_32x32x16_f16 v[98:113], v[138:141], v[154:157], v[98:113]
	v_mfma_f32_32x32x16_f16 v[18:33], v[138:141], v[158:161], v[18:33]
	ds_read_b128 v[138:141], v236 offset:43584
	s_waitcnt lgkmcnt(3)
	v_mfma_f32_32x32x16_f16 v[66:81], v[142:145], v[154:157], v[66:81]
	v_mfma_f32_32x32x16_f16 v[2:17], v[142:145], v[158:161], v[2:17]
	ds_read_b128 v[142:145], v236 offset:47936
	s_waitcnt vmcnt(10)
	s_waitcnt lgkmcnt(3)
	v_mfma_f32_32x32x16_f16 v[82:97], v[130:133], v[162:165], v[82:97]
	v_mfma_f32_32x32x16_f16 v[50:65], v[130:133], v[166:169], v[50:65]
	ds_read_b128 v[130:133], v236 offset:34912
	s_waitcnt lgkmcnt(3)
	v_mfma_f32_32x32x16_f16 v[114:129], v[134:137], v[162:165], v[114:129]
	v_mfma_f32_32x32x16_f16 v[34:49], v[134:137], v[166:169], v[34:49]
	ds_read_b128 v[134:137], v236 offset:39264
	s_waitcnt lgkmcnt(3)
	v_mfma_f32_32x32x16_f16 v[98:113], v[138:141], v[162:165], v[98:113]
	v_mfma_f32_32x32x16_f16 v[18:33], v[138:141], v[166:169], v[18:33]
	ds_read_b128 v[138:141], v236 offset:43616
	s_waitcnt lgkmcnt(3)
	v_mfma_f32_32x32x16_f16 v[66:81], v[142:145], v[162:165], v[66:81]
	v_mfma_f32_32x32x16_f16 v[2:17], v[142:145], v[166:169], v[2:17]
	ds_read_b128 v[142:145], v236 offset:47968
	s_waitcnt vmcnt(8)
	s_waitcnt lgkmcnt(3)
	v_mfma_f32_32x32x16_f16 v[82:97], v[130:133], v[170:173], v[82:97]
	v_mfma_f32_32x32x16_f16 v[50:65], v[130:133], v[174:177], v[50:65]
	ds_read_b128 v[130:133], v236 offset:34944
	s_waitcnt lgkmcnt(3)
	v_mfma_f32_32x32x16_f16 v[114:129], v[134:137], v[170:173], v[114:129]
	v_mfma_f32_32x32x16_f16 v[34:49], v[134:137], v[174:177], v[34:49]
	ds_read_b128 v[134:137], v236 offset:39296
	s_waitcnt lgkmcnt(3)
	v_mfma_f32_32x32x16_f16 v[98:113], v[138:141], v[170:173], v[98:113]
	v_mfma_f32_32x32x16_f16 v[18:33], v[138:141], v[174:177], v[18:33]
	ds_read_b128 v[138:141], v236 offset:43648
	s_waitcnt lgkmcnt(3)
	v_mfma_f32_32x32x16_f16 v[66:81], v[142:145], v[170:173], v[66:81]
	v_mfma_f32_32x32x16_f16 v[2:17], v[142:145], v[174:177], v[2:17]
	ds_read_b128 v[142:145], v236 offset:48000
	s_waitcnt vmcnt(6)
	s_waitcnt lgkmcnt(3)
	v_mfma_f32_32x32x16_f16 v[82:97], v[130:133], v[178:181], v[82:97]
	v_mfma_f32_32x32x16_f16 v[50:65], v[130:133], v[182:185], v[50:65]
	ds_read_b128 v[130:133], v236 offset:34976
	s_waitcnt lgkmcnt(3)
	v_mfma_f32_32x32x16_f16 v[114:129], v[134:137], v[178:181], v[114:129]
	v_mfma_f32_32x32x16_f16 v[34:49], v[134:137], v[182:185], v[34:49]
	ds_read_b128 v[134:137], v236 offset:39328
	s_waitcnt lgkmcnt(3)
	v_mfma_f32_32x32x16_f16 v[98:113], v[138:141], v[178:181], v[98:113]
	v_mfma_f32_32x32x16_f16 v[18:33], v[138:141], v[182:185], v[18:33]
	ds_read_b128 v[138:141], v236 offset:43680
	s_waitcnt lgkmcnt(3)
	v_mfma_f32_32x32x16_f16 v[66:81], v[142:145], v[178:181], v[66:81]
	v_mfma_f32_32x32x16_f16 v[2:17], v[142:145], v[182:185], v[2:17]
	ds_read_b128 v[142:145], v236 offset:48032
	s_waitcnt vmcnt(4)
	s_waitcnt lgkmcnt(3)
	v_mfma_f32_32x32x16_f16 v[82:97], v[130:133], v[186:189], v[82:97]
	v_mfma_f32_32x32x16_f16 v[50:65], v[130:133], v[190:193], v[50:65]
	ds_read_b128 v[130:133], v236 offset:35008
	s_waitcnt lgkmcnt(3)
	v_mfma_f32_32x32x16_f16 v[114:129], v[134:137], v[186:189], v[114:129]
	v_mfma_f32_32x32x16_f16 v[34:49], v[134:137], v[190:193], v[34:49]
	ds_read_b128 v[134:137], v236 offset:39360
	s_waitcnt lgkmcnt(3)
	v_mfma_f32_32x32x16_f16 v[98:113], v[138:141], v[186:189], v[98:113]
	v_mfma_f32_32x32x16_f16 v[18:33], v[138:141], v[190:193], v[18:33]
	ds_read_b128 v[138:141], v236 offset:43712
	s_waitcnt lgkmcnt(3)
	v_mfma_f32_32x32x16_f16 v[66:81], v[142:145], v[186:189], v[66:81]
	v_mfma_f32_32x32x16_f16 v[2:17], v[142:145], v[190:193], v[2:17]
	ds_read_b128 v[142:145], v236 offset:48064
	s_waitcnt vmcnt(2)
	s_waitcnt lgkmcnt(3)
	v_mfma_f32_32x32x16_f16 v[82:97], v[130:133], v[194:197], v[82:97]
	v_mfma_f32_32x32x16_f16 v[50:65], v[130:133], v[198:201], v[50:65]
	ds_read_b128 v[130:133], v236 offset:35040
	s_waitcnt lgkmcnt(3)
	v_mfma_f32_32x32x16_f16 v[114:129], v[134:137], v[194:197], v[114:129]
	v_mfma_f32_32x32x16_f16 v[34:49], v[134:137], v[198:201], v[34:49]
	ds_read_b128 v[134:137], v236 offset:39392
	s_waitcnt lgkmcnt(3)
	v_mfma_f32_32x32x16_f16 v[98:113], v[138:141], v[194:197], v[98:113]
	v_mfma_f32_32x32x16_f16 v[18:33], v[138:141], v[198:201], v[18:33]
	ds_read_b128 v[138:141], v236 offset:43744
	s_waitcnt lgkmcnt(3)
	v_mfma_f32_32x32x16_f16 v[66:81], v[142:145], v[194:197], v[66:81]
	v_mfma_f32_32x32x16_f16 v[2:17], v[142:145], v[198:201], v[2:17]
	ds_read_b128 v[142:145], v236 offset:48096
	s_waitcnt vmcnt(0)
	s_waitcnt lgkmcnt(3)
	v_mfma_f32_32x32x16_f16 v[82:97], v[130:133], v[146:149], v[82:97]
	v_mfma_f32_32x32x16_f16 v[50:65], v[130:133], v[150:153], v[50:65]
	s_waitcnt lgkmcnt(2)
	v_mfma_f32_32x32x16_f16 v[114:129], v[134:137], v[146:149], v[114:129]
	v_mfma_f32_32x32x16_f16 v[34:49], v[134:137], v[150:153], v[34:49]
	s_waitcnt lgkmcnt(1)
	v_mfma_f32_32x32x16_f16 v[98:113], v[138:141], v[146:149], v[98:113]
	v_mfma_f32_32x32x16_f16 v[18:33], v[138:141], v[150:153], v[18:33]
	s_waitcnt lgkmcnt(0)
	v_mfma_f32_32x32x16_f16 v[66:81], v[142:145], v[146:149], v[66:81]
	v_mfma_f32_32x32x16_f16 v[2:17], v[142:145], v[150:153], v[2:17]
	s_waitcnt vmcnt(0) lgkmcnt(0)
	s_nop 15
	s_mov_b64 exec, -1
	v_bfe_u32 v202, v0, 5, 1
	s_lshl_b32 s34, s29, 9
	v_and_b32_e32 v203, 0x1c0, v0
	v_and_b32_e32 v204, 31, v0
	v_or3_b32 v0, s34, v203, v204
	v_lshlrev_b32_e32 v0, 2, v0
	s_waitcnt vmcnt(0) lgkmcnt(0)
	s_barrier
	v_mov_b32_e32 v131, v244
	v_mov_b32_e32 v1, v245
	v_fmamk_f32 v130, v131, 0x80000000, v82
	s_mov_b32 s6, 0x3dcccccd
	s_mov_b32 s7, 0xbdcccccd
	v_fma_f32 v132, v130, s6, 0
	v_fma_f32 v133, v132, s6, 0
	v_fma_f32 v130, -v133, v131, v83
	v_fmac_f32_e32 v132, 0x3dcccccd, v130
	v_fmac_f32_e32 v133, 0x3dcccccd, v132
	v_fma_f32 v130, -v133, v131, v84
	v_fmac_f32_e32 v132, 0x3dcccccd, v130
	v_fmac_f32_e32 v133, 0x3dcccccd, v132
	v_fma_f32 v130, -v133, v131, v85
	v_fmac_f32_e32 v132, 0x3dcccccd, v130
	v_fmac_f32_e32 v133, 0x3dcccccd, v132
	v_fma_f32 v130, -v133, v131, v86
	v_fmac_f32_e32 v132, 0x3dcccccd, v130
	v_fmac_f32_e32 v133, 0x3dcccccd, v132
	v_fma_f32 v130, -v133, v131, v87
	v_fmac_f32_e32 v132, 0x3dcccccd, v130
	v_fmac_f32_e32 v133, 0x3dcccccd, v132
	v_fma_f32 v130, -v133, v131, v88
	v_fmac_f32_e32 v132, 0x3dcccccd, v130
	v_fmac_f32_e32 v133, 0x3dcccccd, v132
	v_fma_f32 v130, -v133, v131, v89
	v_fmac_f32_e32 v132, 0x3dcccccd, v130
	v_fmac_f32_e32 v133, 0x3dcccccd, v132
	v_fma_f32 v130, -v133, v131, v90
	v_fmac_f32_e32 v132, 0x3dcccccd, v130
	v_fmac_f32_e32 v133, 0x3dcccccd, v132
	v_fma_f32 v130, -v133, v131, v91
	v_fmac_f32_e32 v132, 0x3dcccccd, v130
	v_fmac_f32_e32 v133, 0x3dcccccd, v132
	v_fma_f32 v130, -v133, v131, v92
	v_fmac_f32_e32 v132, 0x3dcccccd, v130
	v_fmac_f32_e32 v133, 0x3dcccccd, v132
	v_fma_f32 v130, -v133, v131, v93
	v_fmac_f32_e32 v132, 0x3dcccccd, v130
	v_fmac_f32_e32 v133, 0x3dcccccd, v132
	v_fma_f32 v130, -v133, v131, v94
	v_fmac_f32_e32 v132, 0x3dcccccd, v130
	v_fmac_f32_e32 v133, 0x3dcccccd, v132
	v_fma_f32 v130, -v133, v131, v95
	v_fmac_f32_e32 v132, 0x3dcccccd, v130
	v_fmac_f32_e32 v133, 0x3dcccccd, v132
	v_fma_f32 v130, -v133, v131, v96
	v_fmac_f32_e32 v132, 0x3dcccccd, v130
	v_fmac_f32_e32 v133, 0x3dcccccd, v132
	v_fma_f32 v130, -v133, v131, v97
	v_fmac_f32_e32 v132, 0x3dcccccd, v130
	v_fmac_f32_e32 v133, 0x3dcccccd, v132
	v_fma_f32 v130, -v133, v131, v114
	v_fmac_f32_e32 v132, 0x3dcccccd, v130
	v_fmac_f32_e32 v133, 0x3dcccccd, v132
	v_fma_f32 v130, -v133, v131, v115
	v_fmac_f32_e32 v132, 0x3dcccccd, v130
	v_fmac_f32_e32 v133, 0x3dcccccd, v132
	v_fma_f32 v130, -v133, v131, v116
	v_fmac_f32_e32 v132, 0x3dcccccd, v130
	v_fmac_f32_e32 v133, 0x3dcccccd, v132
	v_fma_f32 v130, -v133, v131, v117
	v_fmac_f32_e32 v132, 0x3dcccccd, v130
	v_fmac_f32_e32 v133, 0x3dcccccd, v132
	v_fma_f32 v130, -v133, v131, v118
	v_fmac_f32_e32 v132, 0x3dcccccd, v130
	v_fmac_f32_e32 v133, 0x3dcccccd, v132
	v_fma_f32 v130, -v133, v131, v119
	v_fmac_f32_e32 v132, 0x3dcccccd, v130
	v_fmac_f32_e32 v133, 0x3dcccccd, v132
	v_fma_f32 v130, -v133, v131, v120
	v_fmac_f32_e32 v132, 0x3dcccccd, v130
	v_fmac_f32_e32 v133, 0x3dcccccd, v132
	v_fma_f32 v130, -v133, v131, v121
	v_fmac_f32_e32 v132, 0x3dcccccd, v130
	v_fmac_f32_e32 v133, 0x3dcccccd, v132
	v_fma_f32 v130, -v133, v131, v122
	v_fmac_f32_e32 v132, 0x3dcccccd, v130
	v_fmac_f32_e32 v133, 0x3dcccccd, v132
	v_fma_f32 v130, -v133, v131, v123
	v_fmac_f32_e32 v132, 0x3dcccccd, v130
	v_fmac_f32_e32 v133, 0x3dcccccd, v132
	v_fma_f32 v130, -v133, v131, v124
	v_fmac_f32_e32 v132, 0x3dcccccd, v130
	v_fmac_f32_e32 v133, 0x3dcccccd, v132
	v_fma_f32 v130, -v133, v131, v125
	v_fmac_f32_e32 v132, 0x3dcccccd, v130
	v_fmac_f32_e32 v133, 0x3dcccccd, v132
	v_fma_f32 v130, -v133, v131, v126
	v_fmac_f32_e32 v132, 0x3dcccccd, v130
	v_fmac_f32_e32 v133, 0x3dcccccd, v132
	v_fma_f32 v130, -v133, v131, v127
	v_fmac_f32_e32 v132, 0x3dcccccd, v130
	v_fmac_f32_e32 v133, 0x3dcccccd, v132
	v_fma_f32 v130, -v133, v131, v128
	v_fmac_f32_e32 v132, 0x3dcccccd, v130
	v_fmac_f32_e32 v133, 0x3dcccccd, v132
	v_fma_f32 v130, -v133, v131, v129
	v_fmac_f32_e32 v132, 0x3dcccccd, v130
	v_fmac_f32_e32 v133, 0x3dcccccd, v132
	v_fma_f32 v130, -v133, v131, v98
	v_fmac_f32_e32 v132, 0x3dcccccd, v130
	v_fmac_f32_e32 v133, 0x3dcccccd, v132
	v_fma_f32 v130, -v133, v131, v99
	v_fmac_f32_e32 v132, 0x3dcccccd, v130
	v_fmac_f32_e32 v133, 0x3dcccccd, v132
	v_fma_f32 v130, -v133, v131, v100
	v_fmac_f32_e32 v132, 0x3dcccccd, v130
	v_fmac_f32_e32 v133, 0x3dcccccd, v132
	v_fma_f32 v130, -v133, v131, v101
	v_fmac_f32_e32 v132, 0x3dcccccd, v130
	v_fmac_f32_e32 v133, 0x3dcccccd, v132
	v_fma_f32 v130, -v133, v131, v102
	v_fmac_f32_e32 v132, 0x3dcccccd, v130
	v_fmac_f32_e32 v133, 0x3dcccccd, v132
	v_fma_f32 v130, -v133, v131, v103
	v_fmac_f32_e32 v132, 0x3dcccccd, v130
	v_fmac_f32_e32 v133, 0x3dcccccd, v132
	v_fma_f32 v130, -v133, v131, v104
	v_fmac_f32_e32 v132, 0x3dcccccd, v130
	v_fmac_f32_e32 v133, 0x3dcccccd, v132
	v_fma_f32 v130, -v133, v131, v105
	v_fmac_f32_e32 v132, 0x3dcccccd, v130
	v_fmac_f32_e32 v133, 0x3dcccccd, v132
	v_fma_f32 v130, -v133, v131, v106
	v_fmac_f32_e32 v132, 0x3dcccccd, v130
	v_fmac_f32_e32 v133, 0x3dcccccd, v132
	v_fma_f32 v130, -v133, v131, v107
	v_fmac_f32_e32 v132, 0x3dcccccd, v130
	v_fmac_f32_e32 v133, 0x3dcccccd, v132
	v_fma_f32 v130, -v133, v131, v108
	v_fmac_f32_e32 v132, 0x3dcccccd, v130
	v_fmac_f32_e32 v133, 0x3dcccccd, v132
	v_fma_f32 v130, -v133, v131, v109
	v_fmac_f32_e32 v132, 0x3dcccccd, v130
	v_fmac_f32_e32 v133, 0x3dcccccd, v132
	v_fma_f32 v130, -v133, v131, v110
	v_fmac_f32_e32 v132, 0x3dcccccd, v130
	v_fmac_f32_e32 v133, 0x3dcccccd, v132
	v_fma_f32 v130, -v133, v131, v111
	v_fmac_f32_e32 v132, 0x3dcccccd, v130
	v_fmac_f32_e32 v133, 0x3dcccccd, v132
	v_fma_f32 v130, -v133, v131, v112
	v_fmac_f32_e32 v132, 0x3dcccccd, v130
	v_fmac_f32_e32 v133, 0x3dcccccd, v132
	v_fma_f32 v130, -v133, v131, v113
	v_fmac_f32_e32 v132, 0x3dcccccd, v130
	v_fmac_f32_e32 v133, 0x3dcccccd, v132
	v_fma_f32 v130, -v133, v131, v66
	v_fmac_f32_e32 v132, 0x3dcccccd, v130
	v_fmac_f32_e32 v133, 0x3dcccccd, v132
	v_fma_f32 v130, -v133, v131, v67
	v_fmac_f32_e32 v132, 0x3dcccccd, v130
	v_fmac_f32_e32 v133, 0x3dcccccd, v132
	v_fma_f32 v130, -v133, v131, v68
	v_fmac_f32_e32 v132, 0x3dcccccd, v130
	v_fmac_f32_e32 v133, 0x3dcccccd, v132
	v_fma_f32 v130, -v133, v131, v69
	v_fmac_f32_e32 v132, 0x3dcccccd, v130
	v_fmac_f32_e32 v133, 0x3dcccccd, v132
	v_fma_f32 v130, -v133, v131, v70
	v_fmac_f32_e32 v132, 0x3dcccccd, v130
	v_fmac_f32_e32 v133, 0x3dcccccd, v132
	v_fma_f32 v130, -v133, v131, v71
	v_fmac_f32_e32 v132, 0x3dcccccd, v130
	v_fmac_f32_e32 v133, 0x3dcccccd, v132
	v_fma_f32 v130, -v133, v131, v72
	v_fmac_f32_e32 v132, 0x3dcccccd, v130
	v_fmac_f32_e32 v133, 0x3dcccccd, v132
	v_fma_f32 v130, -v133, v131, v73
	v_fmac_f32_e32 v132, 0x3dcccccd, v130
	v_fmac_f32_e32 v133, 0x3dcccccd, v132
	v_fma_f32 v130, -v133, v131, v74
	v_fmac_f32_e32 v132, 0x3dcccccd, v130
	v_fmac_f32_e32 v133, 0x3dcccccd, v132
	v_fma_f32 v130, -v133, v131, v75
	v_fmac_f32_e32 v132, 0x3dcccccd, v130
	v_fmac_f32_e32 v133, 0x3dcccccd, v132
	v_fma_f32 v130, -v133, v131, v76
	v_fmac_f32_e32 v132, 0x3dcccccd, v130
	v_fmac_f32_e32 v133, 0x3dcccccd, v132
	v_fma_f32 v130, -v133, v131, v77
	v_fmac_f32_e32 v132, 0x3dcccccd, v130
	v_fmac_f32_e32 v133, 0x3dcccccd, v132
	v_fma_f32 v130, -v133, v131, v78
	v_fmac_f32_e32 v132, 0x3dcccccd, v130
	v_fmac_f32_e32 v133, 0x3dcccccd, v132
	v_fma_f32 v130, -v133, v131, v79
	v_fmac_f32_e32 v132, 0x3dcccccd, v130
	v_fmac_f32_e32 v133, 0x3dcccccd, v132
	v_fma_f32 v130, -v133, v131, v80
	v_fmac_f32_e32 v132, 0x3dcccccd, v130
	v_fmac_f32_e32 v133, 0x3dcccccd, v132
	v_fma_f32 v130, -v133, v131, v81
	v_fmac_f32_e32 v132, 0x3dcccccd, v130
	v_fmamk_f32 v130, v1, 0x80000000, v50
	v_fma_f32 v134, v130, s6, 0
	v_fma_f32 v135, v134, s6, 0
	v_fma_f32 v130, -v135, v1, v51
	v_fmac_f32_e32 v134, 0x3dcccccd, v130
	v_fmac_f32_e32 v135, 0x3dcccccd, v134
	v_fma_f32 v130, -v135, v1, v52
	v_fmac_f32_e32 v134, 0x3dcccccd, v130
	v_fmac_f32_e32 v135, 0x3dcccccd, v134
	v_fma_f32 v130, -v135, v1, v53
	v_fmac_f32_e32 v134, 0x3dcccccd, v130
	v_fmac_f32_e32 v135, 0x3dcccccd, v134
	v_fma_f32 v130, -v135, v1, v54
	v_fmac_f32_e32 v134, 0x3dcccccd, v130
	v_fmac_f32_e32 v135, 0x3dcccccd, v134
	v_fma_f32 v130, -v135, v1, v55
	v_fmac_f32_e32 v134, 0x3dcccccd, v130
	v_fmac_f32_e32 v135, 0x3dcccccd, v134
	v_fma_f32 v130, -v135, v1, v56
	v_fmac_f32_e32 v134, 0x3dcccccd, v130
	v_fmac_f32_e32 v135, 0x3dcccccd, v134
	v_fma_f32 v130, -v135, v1, v57
	v_fmac_f32_e32 v134, 0x3dcccccd, v130
	v_fmac_f32_e32 v135, 0x3dcccccd, v134
	v_fma_f32 v130, -v135, v1, v58
	v_fmac_f32_e32 v134, 0x3dcccccd, v130
	v_fmac_f32_e32 v135, 0x3dcccccd, v134
	v_fma_f32 v130, -v135, v1, v59
	v_fmac_f32_e32 v134, 0x3dcccccd, v130
	v_fmac_f32_e32 v135, 0x3dcccccd, v134
	v_fma_f32 v130, -v135, v1, v60
	v_fmac_f32_e32 v134, 0x3dcccccd, v130
	v_fmac_f32_e32 v135, 0x3dcccccd, v134
	v_fma_f32 v130, -v135, v1, v61
	v_fmac_f32_e32 v134, 0x3dcccccd, v130
	v_fmac_f32_e32 v135, 0x3dcccccd, v134
	v_fma_f32 v130, -v135, v1, v62
	v_fmac_f32_e32 v134, 0x3dcccccd, v130
	v_fmac_f32_e32 v135, 0x3dcccccd, v134
	v_fma_f32 v130, -v135, v1, v63
	v_fmac_f32_e32 v134, 0x3dcccccd, v130
	v_fmac_f32_e32 v135, 0x3dcccccd, v134
	v_fma_f32 v130, -v135, v1, v64
	v_fmac_f32_e32 v134, 0x3dcccccd, v130
	v_fmac_f32_e32 v135, 0x3dcccccd, v134
	v_fma_f32 v130, -v135, v1, v65
	v_fmac_f32_e32 v134, 0x3dcccccd, v130
	v_fmac_f32_e32 v135, 0x3dcccccd, v134
	v_fma_f32 v130, -v135, v1, v34
	v_fmac_f32_e32 v134, 0x3dcccccd, v130
	v_fmac_f32_e32 v135, 0x3dcccccd, v134
	v_fma_f32 v130, -v135, v1, v35
	v_fmac_f32_e32 v134, 0x3dcccccd, v130
	v_fmac_f32_e32 v135, 0x3dcccccd, v134
	v_fma_f32 v130, -v135, v1, v36
	v_fmac_f32_e32 v134, 0x3dcccccd, v130
	v_fmac_f32_e32 v135, 0x3dcccccd, v134
	v_fma_f32 v130, -v135, v1, v37
	v_fmac_f32_e32 v134, 0x3dcccccd, v130
	v_fmac_f32_e32 v135, 0x3dcccccd, v134
	v_fma_f32 v130, -v135, v1, v38
	v_fmac_f32_e32 v134, 0x3dcccccd, v130
	v_fmac_f32_e32 v135, 0x3dcccccd, v134
	v_fma_f32 v130, -v135, v1, v39
	v_fmac_f32_e32 v134, 0x3dcccccd, v130
	v_fmac_f32_e32 v135, 0x3dcccccd, v134
	v_fma_f32 v130, -v135, v1, v40
	v_fmac_f32_e32 v134, 0x3dcccccd, v130
	v_fmac_f32_e32 v135, 0x3dcccccd, v134
	v_fma_f32 v130, -v135, v1, v41
	v_fmac_f32_e32 v134, 0x3dcccccd, v130
	v_fmac_f32_e32 v135, 0x3dcccccd, v134
	v_fma_f32 v130, -v135, v1, v42
	v_fmac_f32_e32 v134, 0x3dcccccd, v130
	v_fmac_f32_e32 v135, 0x3dcccccd, v134
	v_fma_f32 v130, -v135, v1, v43
	v_fmac_f32_e32 v134, 0x3dcccccd, v130
	v_fmac_f32_e32 v135, 0x3dcccccd, v134
	v_fma_f32 v130, -v135, v1, v44
	v_fmac_f32_e32 v134, 0x3dcccccd, v130
	v_fmac_f32_e32 v135, 0x3dcccccd, v134
	v_fma_f32 v130, -v135, v1, v45
	v_fmac_f32_e32 v134, 0x3dcccccd, v130
	v_fmac_f32_e32 v135, 0x3dcccccd, v134
	v_fma_f32 v130, -v135, v1, v46
	v_fmac_f32_e32 v134, 0x3dcccccd, v130
	v_fmac_f32_e32 v135, 0x3dcccccd, v134
	v_fma_f32 v130, -v135, v1, v47
	v_fmac_f32_e32 v134, 0x3dcccccd, v130
	v_fmac_f32_e32 v135, 0x3dcccccd, v134
	v_fma_f32 v130, -v135, v1, v48
	v_fmac_f32_e32 v134, 0x3dcccccd, v130
	v_fmac_f32_e32 v135, 0x3dcccccd, v134
	v_fma_f32 v130, -v135, v1, v49
	v_fmac_f32_e32 v134, 0x3dcccccd, v130
	v_fmac_f32_e32 v135, 0x3dcccccd, v134
	v_fma_f32 v130, -v135, v1, v18
	v_fmac_f32_e32 v134, 0x3dcccccd, v130
	v_fmac_f32_e32 v135, 0x3dcccccd, v134
	v_fma_f32 v130, -v135, v1, v19
	v_fmac_f32_e32 v134, 0x3dcccccd, v130
	v_fmac_f32_e32 v135, 0x3dcccccd, v134
	v_fma_f32 v130, -v135, v1, v20
	v_fmac_f32_e32 v134, 0x3dcccccd, v130
	v_fmac_f32_e32 v135, 0x3dcccccd, v134
	v_fma_f32 v130, -v135, v1, v21
	v_fmac_f32_e32 v134, 0x3dcccccd, v130
	v_fmac_f32_e32 v135, 0x3dcccccd, v134
	v_fma_f32 v130, -v135, v1, v22
	v_fmac_f32_e32 v134, 0x3dcccccd, v130
	v_fmac_f32_e32 v135, 0x3dcccccd, v134
	v_fma_f32 v130, -v135, v1, v23
	v_fmac_f32_e32 v134, 0x3dcccccd, v130
	v_fmac_f32_e32 v135, 0x3dcccccd, v134
	v_fma_f32 v130, -v135, v1, v24
	v_fmac_f32_e32 v134, 0x3dcccccd, v130
	v_fmac_f32_e32 v135, 0x3dcccccd, v134
	v_fma_f32 v130, -v135, v1, v25
	v_fmac_f32_e32 v134, 0x3dcccccd, v130
	v_fmac_f32_e32 v135, 0x3dcccccd, v134
	v_fma_f32 v130, -v135, v1, v26
	v_fmac_f32_e32 v134, 0x3dcccccd, v130
	v_fmac_f32_e32 v135, 0x3dcccccd, v134
	v_fma_f32 v130, -v135, v1, v27
	v_fmac_f32_e32 v134, 0x3dcccccd, v130
	v_fmac_f32_e32 v135, 0x3dcccccd, v134
	v_fma_f32 v130, -v135, v1, v28
	v_fmac_f32_e32 v134, 0x3dcccccd, v130
	v_fmac_f32_e32 v135, 0x3dcccccd, v134
	v_fma_f32 v130, -v135, v1, v29
	v_fmac_f32_e32 v134, 0x3dcccccd, v130
	v_fmac_f32_e32 v135, 0x3dcccccd, v134
	v_fma_f32 v130, -v135, v1, v30
	v_fmac_f32_e32 v134, 0x3dcccccd, v130
	v_fmac_f32_e32 v135, 0x3dcccccd, v134
	v_fma_f32 v130, -v135, v1, v31
	v_fmac_f32_e32 v134, 0x3dcccccd, v130
	v_fmac_f32_e32 v135, 0x3dcccccd, v134
	v_fma_f32 v130, -v135, v1, v32
	v_fmac_f32_e32 v134, 0x3dcccccd, v130
	v_fmac_f32_e32 v135, 0x3dcccccd, v134
	v_fma_f32 v130, -v135, v1, v33
	v_fmac_f32_e32 v134, 0x3dcccccd, v130
	v_fmac_f32_e32 v135, 0x3dcccccd, v134
	v_fma_f32 v130, -v135, v1, v2
	v_fmac_f32_e32 v134, 0x3dcccccd, v130
	v_fmac_f32_e32 v135, 0x3dcccccd, v134
	v_fma_f32 v130, -v135, v1, v3
	v_fmac_f32_e32 v134, 0x3dcccccd, v130
	v_fmac_f32_e32 v135, 0x3dcccccd, v134
	v_fma_f32 v130, -v135, v1, v4
	v_fmac_f32_e32 v134, 0x3dcccccd, v130
	v_fmac_f32_e32 v135, 0x3dcccccd, v134
	v_fma_f32 v130, -v135, v1, v5
	v_fmac_f32_e32 v134, 0x3dcccccd, v130
	v_fmac_f32_e32 v135, 0x3dcccccd, v134
	v_fma_f32 v130, -v135, v1, v6
	v_fmac_f32_e32 v134, 0x3dcccccd, v130
	v_fmac_f32_e32 v135, 0x3dcccccd, v134
	v_fma_f32 v130, -v135, v1, v7
	v_fmac_f32_e32 v134, 0x3dcccccd, v130
	v_fmac_f32_e32 v135, 0x3dcccccd, v134
	v_fma_f32 v130, -v135, v1, v8
	v_fmac_f32_e32 v134, 0x3dcccccd, v130
	v_fmac_f32_e32 v135, 0x3dcccccd, v134
	v_fma_f32 v130, -v135, v1, v9
	v_fmac_f32_e32 v134, 0x3dcccccd, v130
	v_fmac_f32_e32 v135, 0x3dcccccd, v134
	v_fma_f32 v130, -v135, v1, v10
	v_fmac_f32_e32 v134, 0x3dcccccd, v130
	v_fmac_f32_e32 v135, 0x3dcccccd, v134
	v_fma_f32 v130, -v135, v1, v11
	v_fmac_f32_e32 v134, 0x3dcccccd, v130
	v_fmac_f32_e32 v135, 0x3dcccccd, v134
	v_fma_f32 v130, -v135, v1, v12
	v_fmac_f32_e32 v134, 0x3dcccccd, v130
	v_fmac_f32_e32 v135, 0x3dcccccd, v134
	v_fma_f32 v130, -v135, v1, v13
	v_fmac_f32_e32 v134, 0x3dcccccd, v130
	v_fmac_f32_e32 v135, 0x3dcccccd, v134
	v_fma_f32 v130, -v135, v1, v14
	v_fmac_f32_e32 v134, 0x3dcccccd, v130
	v_fmac_f32_e32 v135, 0x3dcccccd, v134
	v_fma_f32 v130, -v135, v1, v15
	v_fmac_f32_e32 v134, 0x3dcccccd, v130
	v_fmac_f32_e32 v135, 0x3dcccccd, v134
	v_fma_f32 v130, -v135, v1, v16
	v_fmac_f32_e32 v134, 0x3dcccccd, v130
	v_fmac_f32_e32 v135, 0x3dcccccd, v134
	v_lshlrev_b32_e32 v142, 3, v203
	v_lshlrev_b32_e32 v140, 3, v204
	v_fma_f32 v130, -v135, v1, v17
	v_add3_u32 v150, 0, v142, v140
	v_fmac_f32_e32 v134, 0x3dcccccd, v130
	s_mov_b32 s10, 0xbc23d70b
	v_lshl_add_u32 v0, v202, 12, v150
	v_fmac_f32_e32 v133, 0x3dcccccd, v132
	v_fmac_f32_e32 v135, 0x3dcccccd, v134
	v_fma_f32 v130, v131, s10, 1.0
	ds_write2_b64 v0, v[132:133], v[134:135] offset1:32
	v_pk_mul_f32 v[132:133], v[130:131], s[6:7]
	s_lshl_b64 s[2:3], s[2:3], 13
	v_mov_b32_e32 v132, v130
	v_pk_mul_f32 v[136:137], v[132:133], s[6:7] op_sel_hi:[1,0]
	v_pk_mul_f32 v[138:139], v[130:131], v[132:133] op_sel_hi:[0,1]
	v_add_f32_e32 v0, 1.0, v137
	v_mov_b32_e32 v136, v137
	v_mov_b32_e32 v137, v133
	v_pk_fma_f32 v[144:145], v[130:131], v[132:133], v[136:137] op_sel_hi:[0,1,1]
	v_mov_b32_e32 v136, 0x3dcccccd
	v_mov_b32_e32 v137, v139
	v_pk_fma_f32 v[146:147], v[130:131], s[6:7], v[136:137]
	v_mov_b32_e32 v137, v138
	v_pk_fma_f32 v[132:133], v[132:133], s[6:7], v[136:137] op_sel_hi:[1,0,1]
	v_mov_b32_e32 v152, v144
	v_pk_mul_f32 v[132:133], v[144:145], v[132:133]
	v_mov_b32_e32 v145, v147
	v_mov_b32_e32 v153, v146
	v_mov_b32_e32 v138, v147
	v_mov_b32_e32 v139, v0
	v_mov_b32_e32 v148, v146
	v_mov_b32_e32 v149, v0
	v_pk_mul_f32 v[144:145], v[144:145], v[152:153]
	v_pk_fma_f32 v[132:133], v[0:1], v[146:147], v[132:133] op_sel_hi:[0,1,1]
	v_pk_fma_f32 v[138:139], v[138:139], v[148:149], v[144:145]
	s_add_u32 s8, s4, s2
	v_pk_mul_f32 v[144:145], v[132:133], v[138:139] op_sel_hi:[1,0]
	s_waitcnt lgkmcnt(0)
	v_pk_fma_f32 v[144:145], v[138:139], v[132:133], v[144:145] op_sel:[1,0,0]
	v_pk_mul_f32 v[132:133], v[132:133], v[132:133] op_sel:[1,0] op_sel_hi:[1,0]
	s_barrier
	v_pk_fma_f32 v[132:133], v[138:139], v[138:139], v[132:133]
	s_nop 0
	v_pk_mul_f32 v[138:139], v[144:145], v[132:133] op_sel_hi:[1,0]
	s_addc_u32 s3, s5, s3
	v_pk_fma_f32 v[138:139], v[132:133], v[144:145], v[138:139] op_sel:[1,0,0]
	v_pk_mul_f32 v[144:145], v[144:145], v[144:145] op_sel:[1,0] op_sel_hi:[1,0]
	s_lshl_b32 s2, s34, 3
	v_pk_fma_f32 v[132:133], v[132:133], v[132:133], v[144:145]
	ds_read_b64 v[148:149], v150
	v_pk_mul_f32 v[144:145], v[138:139], v[132:133] op_sel_hi:[1,0]
	s_add_u32 s8, s8, s2
	v_pk_fma_f32 v[144:145], v[132:133], v[138:139], v[144:145] op_sel:[1,0,0]
	v_pk_mul_f32 v[138:139], v[138:139], v[138:139] op_sel:[1,0] op_sel_hi:[1,0]
	v_mov_b32_e32 v143, 0
	v_pk_fma_f32 v[132:133], v[132:133], v[132:133], v[138:139]
	s_addc_u32 s9, s3, 0
	v_pk_mul_f32 v[138:139], v[132:133], v[132:133]
	v_pk_mul_f32 v[146:147], v[144:145], v[132:133] op_sel_hi:[1,0]
	v_mov_b32_e32 v141, v143
	v_pk_fma_f32 v[132:133], v[132:133], v[144:145], v[146:147] op_sel:[1,0,0]
	v_pk_fma_f32 v[146:147], v[144:145], v[144:145], v[138:139] op_sel:[1,0,0] op_sel_hi:[1,0,1]
	v_lshl_add_u64 v[138:139], s[8:9], 0, v[142:143]
	v_mov_b32_e32 v135, 1.0
	v_cmp_eq_u32_e64 s[0:1], 0, v202
	v_cmp_ne_u32_e32 vcc, 0, v202
	v_lshl_add_u64 v[144:145], v[138:139], 0, v[140:141]
	s_and_saveexec_b64 s[8:9], vcc
	s_cbranch_execz .LBB1_18
	ds_read_b64 v[138:139], v150 offset:4096
	v_mov_b32_e32 v152, v147
	v_mov_b32_e32 v153, v133
	s_waitcnt lgkmcnt(1)
	v_pk_mul_f32 v[152:153], v[148:149], v[152:153]
	s_nop 0
	v_add_f32_e32 v0, v152, v153
	v_mov_b32_e32 v152, v132
	v_mov_b32_e32 v153, v146
	v_pk_mul_f32 v[152:153], v[148:149], v[152:153]
	s_waitcnt lgkmcnt(0)
	v_add_f32_e32 v0, v138, v0
	v_add_f32_e32 v130, v152, v153
	v_add_f32_e32 v130, v139, v130
	v_or_b32_e32 v139, 1, v130
	v_or_b32_e32 v138, 1, v0
	global_store_dwordx2 v[144:145], v[138:139], off sc1
